# attention QK fragment batches: single lgkmcnt(0) before the MFMA run replaced by counted lgkmcnt waits per MFMA (first MFMA starts when its own K fragment has arrived)
# speedup vs baseline: 1.0059x; 1.0018x over previous
.LBB0_940:
	s_cmp_gt_i32 s52, s9
	s_cbranch_scc1 .LBB0_924
	s_mul_hi_u32 s6, s61, 0xaaaaaaab
	s_lshr_b32 s6, s6, 1
	s_mul_i32 s6, s6, 0x18000
	v_subrev_u32_e32 v46, s6, v212
	v_subrev_u32_e32 v47, s6, v211
	v_subrev_u32_e32 v48, s6, v210
	v_subrev_u32_e32 v49, s6, v209
	s_add_i32 s30, s52, 63
	v_add_u32_e32 v50, s60, v218
	s_cmp_gt_i32 s52, s8
	v_add_u32_e32 v2, s52, v208
	v_add_u32_e32 v79, v50, v49
	v_add_u32_e32 v78, v50, v48
	v_add_u32_e32 v75, v50, v47
	v_add_u32_e32 v74, v50, v46
	s_cbranch_scc1 .LBB0_945
	ds_read_b128 v[38:41], v79 offset:40960
	ds_read_b128 v[42:45], v79 offset:45056
	ds_read_b128 v[46:49], v78 offset:40960
	ds_read_b128 v[50:53], v78 offset:45056
	ds_read_b128 v[54:57], v75 offset:40960
	ds_read_b128 v[62:65], v75 offset:45056
	ds_read_b128 v[58:61], v74 offset:40960
	ds_read_b128 v[66:69], v74 offset:45056
	s_setprio 1
	s_waitcnt lgkmcnt(7)
	v_mfma_f32_16x16x32_f16 v[38:41], v[38:41], v[6:9], 0
	s_waitcnt lgkmcnt(5)
	v_mfma_f32_16x16x32_f16 v[38:41], v[46:49], v[10:13], v[38:41]
	s_waitcnt lgkmcnt(3)
	v_mfma_f32_16x16x32_f16 v[38:41], v[54:57], v[14:17], v[38:41]
	s_waitcnt lgkmcnt(1)
	v_mfma_f32_16x16x32_f16 v[58:61], v[58:61], v[18:21], v[38:41]
	v_mfma_f32_16x16x32_f16 v[38:41], v[42:45], v[6:9], 0
	v_mfma_f32_16x16x32_f16 v[38:41], v[50:53], v[10:13], v[38:41]
	v_mfma_f32_16x16x32_f16 v[38:41], v[62:65], v[14:17], v[38:41]
	s_waitcnt lgkmcnt(0)
	v_mfma_f32_16x16x32_f16 v[54:57], v[66:69], v[18:21], v[38:41]
	s_setprio 0
	s_nop 5
	ds_read_b128 v[38:41], v79 offset:49152
	ds_read_b128 v[42:45], v79 offset:53248
	ds_read_b128 v[46:49], v78 offset:49152
	ds_read_b128 v[62:65], v78 offset:53248
	ds_read_b128 v[50:53], v75 offset:49152
	ds_read_b128 v[66:69], v75 offset:53248
	ds_read_b128 v[80:83], v74 offset:49152
	ds_read_b128 v[84:87], v74 offset:53248
	s_setprio 1
	s_waitcnt lgkmcnt(7)
	v_mfma_f32_16x16x32_f16 v[38:41], v[38:41], v[6:9], 0
	s_waitcnt lgkmcnt(5)
	v_mfma_f32_16x16x32_f16 v[38:41], v[46:49], v[10:13], v[38:41]
	s_waitcnt lgkmcnt(3)
	v_mfma_f32_16x16x32_f16 v[38:41], v[50:53], v[14:17], v[38:41]
	s_waitcnt lgkmcnt(1)
	v_mfma_f32_16x16x32_f16 v[50:53], v[80:83], v[18:21], v[38:41]
	v_mfma_f32_16x16x32_f16 v[38:41], v[42:45], v[6:9], 0
	v_mfma_f32_16x16x32_f16 v[38:41], v[62:65], v[10:13], v[38:41]
	v_mfma_f32_16x16x32_f16 v[38:41], v[66:69], v[14:17], v[38:41]
	s_waitcnt lgkmcnt(0)
	v_mfma_f32_16x16x32_f16 v[46:49], v[84:87], v[18:21], v[38:41]
	s_setprio 0
	s_cmp_le_i32 s30, s13
	s_cselect_b64 s[6:7], -1, 0
	s_cmpk_gt_i32 s47, 0x9d
	s_cselect_b64 s[34:35], -1, 0
	s_and_b64 s[34:35], s[6:7], s[34:35]
	s_mov_b64 s[6:7], -1
	s_and_b64 vcc, exec, s[34:35]
	s_cbranch_vccnz .LBB0_948
	v_add_u32_e32 v38, s47, v219
	v_add_u32_e32 v39, 0x3f0, v38
	v_add_u32_e32 v40, 0x3e0, v38
	v_add_u32_e32 v42, 0x3d0, v38
	v_add_u32_e32 v44, 0x3c0, v38
	v_add_u32_e32 v62, 0x3b0, v38
	v_add_u32_e32 v64, 0x3a0, v38
	v_add_u32_e32 v66, 0x390, v38
	v_add_u32_e32 v68, 0x380, v38
	v_med3_i32 v39, v39, 31, v240
	v_med3_i32 v40, v40, 31, v240
	v_med3_i32 v42, v42, 31, v240
	v_med3_i32 v44, v44, 31, v240
	v_med3_i32 v62, v62, 31, v240
	v_med3_i32 v64, v64, 31, v240
	v_med3_i32 v66, v66, 31, v240
	v_med3_i32 v68, v68, 31, v240
	v_lshlrev_b32_e32 v39, 2, v39
	v_lshlrev_b32_e32 v40, 2, v40
	v_lshlrev_b32_e32 v42, 2, v42
	v_lshlrev_b32_e32 v44, 2, v44
	v_lshlrev_b32_e32 v62, 2, v62
	v_lshlrev_b32_e32 v64, 2, v64
	v_lshlrev_b32_e32 v66, 2, v66
	v_lshlrev_b32_e32 v68, 2, v68
	v_add3_u32 v39, v244, v39, s59
	v_add3_u32 v40, v244, v40, s59
	v_add3_u32 v42, v244, v42, s59
	v_add3_u32 v44, v244, v44, s59
	v_add3_u32 v62, v244, v62, s59
	v_add3_u32 v64, v244, v64, s59
	v_add3_u32 v66, v244, v66, s59
	v_add3_u32 v68, v244, v68, s59
	ds_read_b32 v39, v39
	ds_read_b32 v40, v40
	ds_read_b32 v42, v42
	ds_read_b32 v44, v44
	ds_read_b32 v62, v62
	ds_read_b32 v64, v64
	ds_read_b32 v66, v66
	ds_read_b32 v72, v68
	v_add_u32_e32 v68, 0x1f0, v38
	v_add_u32_e32 v85, 0x1b0, v38
	v_add_u32_e32 v86, 0x1a0, v38
	v_add_u32_e32 v87, 0x190, v38
	v_med3_i32 v68, v68, 31, v240
	v_add_u32_e32 v69, 0x1e0, v38
	v_add_u32_e32 v80, 0x1d0, v38
	v_add_u32_e32 v81, 0x1c0, v38
	v_med3_i32 v85, v85, 31, v240
	v_med3_i32 v86, v86, 31, v240
	v_med3_i32 v87, v87, 31, v240
	v_add_u32_e32 v38, 0x180, v38
	v_lshlrev_b32_e32 v68, 2, v68
	v_med3_i32 v69, v69, 31, v240
	v_med3_i32 v80, v80, 31, v240
	v_med3_i32 v81, v81, 31, v240
	v_lshlrev_b32_e32 v85, 2, v85
	v_lshlrev_b32_e32 v86, 2, v86
	v_lshlrev_b32_e32 v87, 2, v87
	v_med3_i32 v38, v38, 31, v240
	v_add3_u32 v68, v244, v68, s59
	v_lshlrev_b32_e32 v69, 2, v69
	v_lshlrev_b32_e32 v80, 2, v80
	v_lshlrev_b32_e32 v81, 2, v81
	v_add3_u32 v85, v244, v85, s59
	v_add3_u32 v86, v244, v86, s59
	v_add3_u32 v87, v244, v87, s59
	v_lshlrev_b32_e32 v38, 2, v38
	v_add3_u32 v69, v244, v69, s59
	v_add3_u32 v80, v244, v80, s59
	v_add3_u32 v81, v244, v81, s59
	v_add3_u32 v38, v244, v38, s59
	ds_read_b32 v88, v68
	ds_read_b32 v89, v69
	ds_read_b32 v90, v80
	ds_read_b32 v91, v81
	ds_read_b32 v85, v85
	ds_read_b32 v86, v86
	ds_read_b32 v87, v87
	ds_read_b32 v92, v38
	v_add_u32_e32 v41, 2, v2
	v_add_u32_e32 v45, 4, v2
	v_add_u32_e32 v63, 5, v2
	v_add_u32_e32 v65, 6, v2
	v_add_u32_e32 v67, 7, v2
	v_add_u32_e32 v43, 3, v2
	v_add_u32_e32 v73, 32, v2
	v_add_u32_e32 v82, 33, v2
	v_add_u32_e32 v83, 34, v2
	v_add_u32_e32 v84, 35, v2
	v_add_u32_e32 v93, 36, v2
	v_add_u32_e32 v94, 37, v2
	v_add_u32_e32 v95, 38, v2
	v_add_u32_e32 v96, 39, v2
	s_waitcnt lgkmcnt(0)
	v_fmac_f32_e32 v39, 0x3e0293ee, v58
	v_cmp_le_i32_e32 vcc, v2, v76
	v_fmac_f32_e32 v40, 0x3e0293ee, v59
	v_fmac_f32_e32 v42, 0x3e0293ee, v60
	v_cndmask_b32_e32 v38, v241, v39, vcc
	v_cmp_lt_i32_e32 vcc, v2, v76
	v_fmac_f32_e32 v44, 0x3e0293ee, v61
	v_fmac_f32_e32 v62, 0x3e0293ee, v54
	v_cndmask_b32_e32 v39, v241, v40, vcc
	v_cmp_le_i32_e32 vcc, v41, v76
	v_fmac_f32_e32 v64, 0x3e0293ee, v55
	v_fmac_f32_e32 v66, 0x3e0293ee, v56
	v_cndmask_b32_e32 v41, v241, v42, vcc
	v_cmp_le_i32_e32 vcc, v43, v76
	v_fmac_f32_e32 v72, 0x3e0293ee, v57
	v_fmac_f32_e32 v88, 0x3e0293ee, v50
	v_cndmask_b32_e32 v69, v241, v44, vcc
	v_cmp_le_i32_e32 vcc, v45, v76
	v_fmac_f32_e32 v89, 0x3e0293ee, v51
	v_fmac_f32_e32 v90, 0x3e0293ee, v52
	v_cndmask_b32_e32 v40, v241, v62, vcc
	v_cmp_le_i32_e32 vcc, v63, v76
	v_max_f32_e32 v42, v38, v39
	v_fmac_f32_e32 v91, 0x3e0293ee, v53
	v_cndmask_b32_e32 v68, v241, v64, vcc
	v_cmp_le_i32_e32 vcc, v65, v76
	v_max3_f32 v42, v42, v41, v69
	v_fmac_f32_e32 v85, 0x3e0293ee, v46
	v_cndmask_b32_e32 v80, v241, v66, vcc
	v_cmp_le_i32_e32 vcc, v67, v76
	v_max3_f32 v42, v42, v40, v68
	v_fmac_f32_e32 v86, 0x3e0293ee, v47
	v_cndmask_b32_e32 v81, v241, v72, vcc
	v_cmp_le_i32_e32 vcc, v73, v76
	v_max3_f32 v42, v42, v80, v81
	v_fmac_f32_e32 v87, 0x3e0293ee, v48
	v_cndmask_b32_e32 v44, v241, v88, vcc
	v_cmp_le_i32_e32 vcc, v82, v76
	v_fmac_f32_e32 v92, 0x3e0293ee, v49
	v_add_f32_e32 v43, 0x41000000, v4
	v_cndmask_b32_e32 v45, v241, v89, vcc
	v_cmp_le_i32_e32 vcc, v83, v76
	v_max3_f32 v42, v42, v44, v45
	s_nop 0
	v_cndmask_b32_e32 v63, v241, v90, vcc
	v_cmp_le_i32_e32 vcc, v84, v76
	s_nop 1
	v_cndmask_b32_e32 v65, v241, v91, vcc
	v_cmp_le_i32_e32 vcc, v93, v76
	v_max3_f32 v42, v42, v63, v65
	s_nop 0
	v_cndmask_b32_e32 v62, v241, v85, vcc
	v_cmp_le_i32_e32 vcc, v94, v76
	s_nop 1
	v_cndmask_b32_e32 v64, v241, v86, vcc
	v_cmp_le_i32_e32 vcc, v95, v76
	v_max3_f32 v42, v42, v62, v64
	s_nop 0
	v_cndmask_b32_e32 v66, v241, v87, vcc
	v_cmp_le_i32_e32 vcc, v96, v76
	s_nop 1
	v_cndmask_b32_e32 v67, v241, v92, vcc
	v_max3_f32 v42, v42, v66, v67
	v_cmp_gt_f32_e32 vcc, v42, v43
	s_cbranch_vccz .LBB0_946
	v_and_b32_e32 v72, 64, v242
	v_xor_b32_e32 v43, 16, v242
	v_add_u32_e32 v72, 64, v72
	v_cmp_lt_i32_e32 vcc, v43, v72
	v_xor_b32_e32 v73, 32, v242
	s_nop 0
	v_cndmask_b32_e32 v43, v242, v43, vcc
	v_lshlrev_b32_e32 v43, 2, v43
	ds_bpermute_b32 v43, v43, v42
	v_max_f32_e32 v42, v42, v42
	v_cmp_lt_i32_e32 vcc, v73, v72
	s_waitcnt lgkmcnt(0)
	v_max_f32_e32 v43, v43, v43
	v_max_f32_e32 v42, v42, v43
	v_cndmask_b32_e32 v43, v242, v73, vcc
	v_lshlrev_b32_e32 v43, 2, v43
	ds_bpermute_b32 v43, v43, v42
	s_waitcnt lgkmcnt(0)
	v_max3_f32 v42, v4, v42, v43
	v_sub_f32_e32 v43, v4, v42
	v_exp_f32_e32 v82, v43
	v_mov_b32_e32 v43, v5
	v_mov_b64_e32 v[72:73], v[42:43]
	s_branch .LBB0_947

.LBB0_954:
	ds_read_b128 v[46:49], v79 offset:40960
	ds_read_b128 v[50:53], v79 offset:45056
	ds_read_b128 v[54:57], v78 offset:40960
	ds_read_b128 v[58:61], v78 offset:45056
	ds_read_b128 v[62:65], v75 offset:40960
	ds_read_b128 v[80:83], v75 offset:45056
	ds_read_b128 v[66:69], v74 offset:40960
	ds_read_b128 v[84:87], v74 offset:45056
	s_setprio 1
	s_waitcnt lgkmcnt(7)
	v_mfma_f32_16x16x32_f16 v[46:49], v[46:49], v[22:25], 0
	s_waitcnt lgkmcnt(5)
	v_mfma_f32_16x16x32_f16 v[46:49], v[54:57], v[26:29], v[46:49]
	s_waitcnt lgkmcnt(3)
	v_mfma_f32_16x16x32_f16 v[46:49], v[62:65], v[30:33], v[46:49]
	s_waitcnt lgkmcnt(1)
	v_mfma_f32_16x16x32_f16 v[66:69], v[66:69], v[34:37], v[46:49]
	v_mfma_f32_16x16x32_f16 v[46:49], v[50:53], v[22:25], 0
	v_mfma_f32_16x16x32_f16 v[46:49], v[58:61], v[26:29], v[46:49]
	v_mfma_f32_16x16x32_f16 v[46:49], v[80:83], v[30:33], v[46:49]
	s_waitcnt lgkmcnt(0)
	v_mfma_f32_16x16x32_f16 v[62:65], v[84:87], v[34:37], v[46:49]
	s_setprio 0
	s_nop 5
	ds_read_b128 v[46:49], v79 offset:49152
	ds_read_b128 v[50:53], v79 offset:53248
	ds_read_b128 v[54:57], v78 offset:49152
	ds_read_b128 v[78:81], v78 offset:53248
	ds_read_b128 v[58:61], v75 offset:49152
	ds_read_b128 v[82:85], v75 offset:53248
	ds_read_b128 v[86:89], v74 offset:49152
	ds_read_b128 v[90:93], v74 offset:53248
	s_setprio 1
	s_waitcnt lgkmcnt(7)
	v_mfma_f32_16x16x32_f16 v[46:49], v[46:49], v[22:25], 0
	s_waitcnt lgkmcnt(5)
	v_mfma_f32_16x16x32_f16 v[46:49], v[54:57], v[26:29], v[46:49]
	s_waitcnt lgkmcnt(3)
	v_mfma_f32_16x16x32_f16 v[46:49], v[58:61], v[30:33], v[46:49]
	s_waitcnt lgkmcnt(1)
	v_mfma_f32_16x16x32_f16 v[58:61], v[86:89], v[34:37], v[46:49]
	v_mfma_f32_16x16x32_f16 v[46:49], v[50:53], v[22:25], 0
	v_mfma_f32_16x16x32_f16 v[46:49], v[78:81], v[26:29], v[46:49]
	v_mfma_f32_16x16x32_f16 v[46:49], v[82:85], v[30:33], v[46:49]
	s_waitcnt lgkmcnt(0)
	v_mfma_f32_16x16x32_f16 v[54:57], v[90:93], v[34:37], v[46:49]
	s_setprio 0
	s_cmp_le_i32 s30, s46
	s_cselect_b64 s[6:7], -1, 0
	s_add_i32 s30, s47, 4
	s_cmpk_gt_i32 s30, 0x9d
	s_cselect_b64 s[30:31], -1, 0
	s_and_b64 s[30:31], s[6:7], s[30:31]
	s_mov_b64 s[6:7], -1
	s_and_b64 vcc, exec, s[30:31]
	s_cbranch_vccnz .LBB0_959
	v_add_u32_e32 v4, s47, v219
	v_add_u32_e32 v5, 0x3f4, v4
	v_add_u32_e32 v46, 0x3e4, v4
	v_add_u32_e32 v47, 0x3d4, v4
	v_add_u32_e32 v48, 0x3c4, v4
	v_add_u32_e32 v52, 0x3b4, v4
	v_add_u32_e32 v74, 0x3a4, v4
	v_add_u32_e32 v78, 0x394, v4
	v_add_u32_e32 v80, 0x384, v4
	v_med3_i32 v5, v5, 31, v240
	v_med3_i32 v46, v46, 31, v240
	v_med3_i32 v47, v47, 31, v240
	v_med3_i32 v48, v48, 31, v240
	v_med3_i32 v52, v52, 31, v240
	v_med3_i32 v74, v74, 31, v240
	v_med3_i32 v78, v78, 31, v240
	v_med3_i32 v80, v80, 31, v240
	v_lshlrev_b32_e32 v5, 2, v5
	v_lshlrev_b32_e32 v46, 2, v46
	v_lshlrev_b32_e32 v47, 2, v47
	v_lshlrev_b32_e32 v48, 2, v48
	v_lshlrev_b32_e32 v52, 2, v52
	v_lshlrev_b32_e32 v74, 2, v74
	v_lshlrev_b32_e32 v78, 2, v78
	v_lshlrev_b32_e32 v80, 2, v80
	v_add3_u32 v5, v244, v5, s59
	v_add3_u32 v46, v244, v46, s59
	v_add3_u32 v47, v244, v47, s59
	v_add3_u32 v48, v244, v48, s59
	v_add3_u32 v52, v244, v52, s59
	v_add3_u32 v74, v244, v74, s59
	v_add3_u32 v78, v244, v78, s59
	v_add3_u32 v80, v244, v80, s59
	ds_read_b32 v5, v5
	ds_read_b32 v46, v46
	ds_read_b32 v81, v47
	ds_read_b32 v82, v48
	ds_read_b32 v52, v52
	ds_read_b32 v74, v74
	ds_read_b32 v78, v78
	ds_read_b32 v80, v80
	v_add_u32_e32 v47, 0x1f4, v4
	v_add_u32_e32 v48, 0x1e4, v4
	v_add_u32_e32 v83, 0x1d4, v4
	v_add_u32_e32 v84, 0x1c4, v4
	v_add_u32_e32 v85, 0x1b4, v4
	v_add_u32_e32 v90, 0x1a4, v4
	v_add_u32_e32 v91, 0x194, v4
	v_add_u32_e32 v4, 0x184, v4
	v_med3_i32 v47, v47, 31, v240
	v_med3_i32 v90, v90, 31, v240
	v_med3_i32 v91, v91, 31, v240
	v_med3_i32 v4, v4, 31, v240
	v_lshlrev_b32_e32 v47, 2, v47
	v_med3_i32 v48, v48, 31, v240
	v_med3_i32 v83, v83, 31, v240
	v_med3_i32 v84, v84, 31, v240
	v_med3_i32 v85, v85, 31, v240
	v_lshlrev_b32_e32 v90, 2, v90
	v_lshlrev_b32_e32 v91, 2, v91
	v_lshlrev_b32_e32 v4, 2, v4
	v_add3_u32 v47, v244, v47, s59
	v_lshlrev_b32_e32 v48, 2, v48
	v_lshlrev_b32_e32 v83, 2, v83
	v_lshlrev_b32_e32 v84, 2, v84
	v_lshlrev_b32_e32 v85, 2, v85
	v_add3_u32 v90, v244, v90, s59
	v_add3_u32 v91, v244, v91, s59
	v_add3_u32 v4, v244, v4, s59
	v_add3_u32 v48, v244, v48, s59
	v_add3_u32 v83, v244, v83, s59
	v_add3_u32 v84, v244, v84, s59
	v_add3_u32 v85, v244, v85, s59
	ds_read_b32 v92, v47
	ds_read_b32 v93, v48
	ds_read_b32 v94, v83
	ds_read_b32 v95, v84
	ds_read_b32 v96, v85
	ds_read_b32 v90, v90
	ds_read_b32 v91, v91
	ds_read_b32 v4, v4
	v_add_u32_e32 v49, 2, v2
	v_add_u32_e32 v53, 5, v2
	v_add_u32_e32 v75, 6, v2
	v_add_u32_e32 v79, 7, v2
	v_add_u32_e32 v50, 3, v2
	v_add_u32_e32 v51, 4, v2
	v_add_u32_e32 v86, 32, v2
	v_add_u32_e32 v87, 33, v2
	v_add_u32_e32 v88, 34, v2
	v_add_u32_e32 v89, 35, v2
	v_add_u32_e32 v97, 36, v2
	v_add_u32_e32 v98, 37, v2
	v_add_u32_e32 v99, 38, v2
	v_add_u32_e32 v100, 39, v2
	s_waitcnt lgkmcnt(0)
	v_fmac_f32_e32 v5, 0x3e0293ee, v66
	v_cmp_le_i32_e32 vcc, v2, v77
	v_fmac_f32_e32 v46, 0x3e0293ee, v67
	v_fmac_f32_e32 v81, 0x3e0293ee, v68
	v_cndmask_b32_e32 v47, v241, v5, vcc
	v_cmp_lt_i32_e32 vcc, v2, v77
	v_fmac_f32_e32 v82, 0x3e0293ee, v69
	v_fmac_f32_e32 v52, 0x3e0293ee, v62
	v_cndmask_b32_e32 v48, v241, v46, vcc
	v_cmp_le_i32_e32 vcc, v49, v77
	v_fmac_f32_e32 v74, 0x3e0293ee, v63
	v_fmac_f32_e32 v78, 0x3e0293ee, v64
	v_cndmask_b32_e32 v81, v241, v81, vcc
	v_cmp_le_i32_e32 vcc, v50, v77
	v_fmac_f32_e32 v80, 0x3e0293ee, v65
	v_fmac_f32_e32 v92, 0x3e0293ee, v58
	v_cndmask_b32_e32 v83, v241, v82, vcc
	v_cmp_le_i32_e32 vcc, v51, v77
	v_fmac_f32_e32 v93, 0x3e0293ee, v59
	v_fmac_f32_e32 v94, 0x3e0293ee, v60
	v_cndmask_b32_e32 v49, v241, v52, vcc
	v_cmp_le_i32_e32 vcc, v53, v77
	v_fmac_f32_e32 v95, 0x3e0293ee, v61
	v_fmac_f32_e32 v96, 0x3e0293ee, v54
	v_cndmask_b32_e32 v82, v241, v74, vcc
	v_cmp_le_i32_e32 vcc, v75, v77
	v_fmac_f32_e32 v90, 0x3e0293ee, v55
	v_fmac_f32_e32 v91, 0x3e0293ee, v56
	v_cndmask_b32_e32 v84, v241, v78, vcc
	v_cmp_le_i32_e32 vcc, v79, v77
	v_fmac_f32_e32 v4, 0x3e0293ee, v57
	v_add_f32_e32 v5, 0x41000000, v73
	v_cndmask_b32_e32 v85, v241, v80, vcc
	v_cmp_le_i32_e32 vcc, v86, v77
	s_nop 1
	v_cndmask_b32_e32 v2, v241, v92, vcc
	v_cmp_le_i32_e32 vcc, v87, v77
	s_nop 1
	v_cndmask_b32_e32 v46, v241, v93, vcc
	v_cmp_le_i32_e32 vcc, v88, v77
	s_nop 1
	v_cndmask_b32_e32 v75, v241, v94, vcc
	v_cmp_le_i32_e32 vcc, v89, v77
	s_nop 1
	v_cndmask_b32_e32 v52, v241, v95, vcc
	v_cmp_le_i32_e32 vcc, v97, v77
	s_nop 1
	v_cndmask_b32_e32 v74, v241, v96, vcc
	v_cmp_le_i32_e32 vcc, v98, v77
	s_nop 1
	v_cndmask_b32_e32 v79, v241, v90, vcc
	v_cmp_le_i32_e32 vcc, v99, v77
	s_nop 1
	v_cndmask_b32_e32 v80, v241, v91, vcc
	v_cmp_le_i32_e32 vcc, v100, v77
	s_nop 1
	v_cndmask_b32_e32 v53, v241, v4, vcc
	v_max_f32_e32 v4, v47, v48
	v_max3_f32 v4, v4, v81, v83
	v_max3_f32 v4, v4, v49, v82
	v_max3_f32 v4, v4, v84, v85
	v_max3_f32 v4, v4, v2, v46
	v_max3_f32 v4, v4, v75, v52
	v_max3_f32 v4, v4, v74, v79
	v_max3_f32 v4, v4, v80, v53
	v_cmp_gt_f32_e32 vcc, v4, v5
	s_cbranch_vccz .LBB0_957
	v_and_b32_e32 v50, 64, v242
	v_xor_b32_e32 v5, 16, v242
	v_add_u32_e32 v50, 64, v50
	v_cmp_lt_i32_e32 vcc, v5, v50
	v_xor_b32_e32 v51, 32, v242
	s_nop 0
	v_cndmask_b32_e32 v5, v242, v5, vcc
	v_lshlrev_b32_e32 v5, 2, v5
	ds_bpermute_b32 v5, v5, v4
	v_max_f32_e32 v4, v4, v4
	v_cmp_lt_i32_e32 vcc, v51, v50
	v_mov_b32_e32 v50, v72
	s_waitcnt lgkmcnt(0)
	v_max_f32_e32 v5, v5, v5
	v_max_f32_e32 v4, v4, v5
	v_cndmask_b32_e32 v5, v242, v51, vcc
	v_lshlrev_b32_e32 v5, 2, v5
	ds_bpermute_b32 v5, v5, v4
	s_waitcnt lgkmcnt(0)
	v_max3_f32 v51, v73, v4, v5
	v_sub_f32_e32 v4, v73, v51
	v_exp_f32_e32 v78, v4
	v_mov_b64_e32 v[4:5], v[50:51]
	s_branch .LBB0_958

.LBB0_981:
	s_cmp_gt_i32 s8, s44
	s_cbranch_scc1 .LBB0_1001
	s_cmp_le_i32 s8, s9
	s_mul_hi_u32 s6, s52, 0xaaaaaaab
	s_cselect_b64 s[30:31], -1, 0
	s_lshr_b32 s34, s6, 1
	s_mul_i32 s34, s34, 0x18000
	v_add_u32_e32 v134, s8, v208
	v_subrev_u32_e32 v149, s34, v232
	v_subrev_u32_e32 v150, s34, v233
	v_subrev_u32_e32 v151, s34, v234
	v_subrev_u32_e32 v152, s34, v235
	v_lshl_or_b32 v188, s51, 6, v208
	s_mov_b64 s[18:19], -1
	s_and_b64 vcc, exec, s[30:31]
	v_add_u32_e32 v135, 4, v134
	v_or_b32_e32 v133, 6, v134
	v_or_b32_e32 v132, 2, v134
	v_add_u32_e32 v160, 3, v134
	v_add_u32_e32 v158, 5, v134
	v_add_u32_e32 v159, 7, v134
	v_or_b32_e32 v131, 36, v134
	v_or_b32_e32 v130, 32, v134
	v_or_b32_e32 v129, 37, v134
	v_or_b32_e32 v128, 33, v134
	v_or_b32_e32 v119, 38, v134
	v_or_b32_e32 v2, 34, v134
	s_cbranch_vccz .LBB0_988
	s_add_i32 s6, s45, s50
	v_add_u32_e32 v153, s6, v152
	v_add_u32_e32 v161, s6, v151
	v_add_u32_e32 v162, s6, v150
	v_add_u32_e32 v163, s6, v149
	ds_read_b128 v[46:49], v153
	ds_read_b128 v[50:53], v153 offset:4096
	ds_read_b128 v[120:123], v161
	ds_read_b128 v[124:127], v161 offset:4096
	ds_read_b128 v[136:139], v162
	ds_read_b128 v[140:143], v162 offset:4096
	ds_read_b128 v[144:147], v163
	ds_read_b128 v[154:157], v163 offset:4096
	s_setprio 1
	s_waitcnt lgkmcnt(7)
	v_mfma_f32_16x16x32_f16 v[46:49], v[46:49], v[6:9], 0
	s_waitcnt lgkmcnt(5)
	v_mfma_f32_16x16x32_f16 v[46:49], v[120:123], v[10:13], v[46:49]
	s_waitcnt lgkmcnt(3)
	v_mfma_f32_16x16x32_f16 v[46:49], v[136:139], v[14:17], v[46:49]
	s_waitcnt lgkmcnt(1)
	v_mfma_f32_16x16x32_f16 v[120:123], v[144:147], v[18:21], v[46:49]
	v_mfma_f32_16x16x32_f16 v[46:49], v[50:53], v[6:9], 0
	v_mfma_f32_16x16x32_f16 v[46:49], v[124:127], v[10:13], v[46:49]
	v_mfma_f32_16x16x32_f16 v[46:49], v[140:143], v[14:17], v[46:49]
	s_waitcnt lgkmcnt(0)
	v_mfma_f32_16x16x32_f16 v[124:127], v[154:157], v[18:21], v[46:49]
	s_setprio 0
	s_nop 5
	ds_read_b128 v[46:49], v153 offset:8192
	ds_read_b128 v[136:139], v153 offset:12288
	ds_read_b128 v[50:53], v161 offset:8192
	ds_read_b128 v[140:143], v161 offset:12288
	ds_read_b128 v[144:147], v162 offset:8192
	ds_read_b128 v[154:157], v162 offset:12288
	ds_read_b128 v[190:193], v163 offset:8192
	ds_read_b128 v[200:203], v163 offset:12288
	s_setprio 1
	s_waitcnt lgkmcnt(7)
	v_mfma_f32_16x16x32_f16 v[46:49], v[46:49], v[6:9], 0
	s_waitcnt lgkmcnt(5)
	v_mfma_f32_16x16x32_f16 v[46:49], v[50:53], v[10:13], v[46:49]
	s_waitcnt lgkmcnt(3)
	v_mfma_f32_16x16x32_f16 v[46:49], v[144:147], v[14:17], v[46:49]
	s_waitcnt lgkmcnt(1)
	v_mfma_f32_16x16x32_f16 v[50:53], v[190:193], v[18:21], v[46:49]
	v_mfma_f32_16x16x32_f16 v[46:49], v[136:139], v[6:9], 0
	v_mfma_f32_16x16x32_f16 v[46:49], v[140:143], v[10:13], v[46:49]
	v_mfma_f32_16x16x32_f16 v[46:49], v[154:157], v[14:17], v[46:49]
	s_waitcnt lgkmcnt(0)
	v_mfma_f32_16x16x32_f16 v[46:49], v[200:203], v[18:21], v[46:49]
	s_setprio 0
	v_lshlrev_b32_e32 v154, 4, v132
	v_lshlrev_b32_e32 v155, 4, v133
	v_lshlrev_b32_e32 v157, 4, v130
	v_add_u32_e32 v136, 0x270, v196
	v_add_u32_e32 v137, 0x260, v196
	v_sub_u32_e32 v138, v185, v154
	v_add_u32_e32 v139, 0x240, v196
	v_add_u32_e32 v140, 0x230, v196
	v_add_u32_e32 v141, 0x220, v196
	v_sub_u32_e32 v142, v185, v155
	v_add_u32_e32 v143, 0x200, v196
	v_sub_u32_e32 v144, v185, v157
	v_lshlrev_b32_e32 v161, 4, v128
	v_lshlrev_b32_e32 v163, 4, v2
	v_lshlrev_b32_e32 v186, 4, v131
	v_lshlrev_b32_e32 v187, 4, v129
	v_lshlrev_b32_e32 v189, 4, v119
	v_med3_i32 v136, v136, 31, v240
	v_med3_i32 v137, v137, 31, v240
	v_med3_i32 v138, v138, 31, v240
	v_med3_i32 v139, v139, 31, v240
	v_med3_i32 v140, v140, 31, v240
	v_med3_i32 v141, v141, 31, v240
	v_med3_i32 v142, v142, 31, v240
	v_med3_i32 v143, v143, 31, v240
	v_med3_i32 v144, v144, 31, v240
	v_sub_u32_e32 v145, v185, v161
	v_sub_u32_e32 v146, v185, v163
	v_add_u32_e32 v147, 64, v196
	v_sub_u32_e32 v153, v185, v186
	v_sub_u32_e32 v156, v185, v187
	v_sub_u32_e32 v162, v185, v189
	v_lshlrev_b32_e32 v136, 2, v136
	v_lshlrev_b32_e32 v137, 2, v137
	v_lshlrev_b32_e32 v138, 2, v138
	v_lshlrev_b32_e32 v139, 2, v139
	v_lshlrev_b32_e32 v140, 2, v140
	v_lshlrev_b32_e32 v141, 2, v141
	v_lshlrev_b32_e32 v142, 2, v142
	v_lshlrev_b32_e32 v143, 2, v143
	v_lshlrev_b32_e32 v144, 2, v144
	v_med3_i32 v145, v145, 31, v240
	v_med3_i32 v146, v146, 31, v240
	v_med3_i32 v147, v147, 31, v240
	v_med3_i32 v153, v153, 31, v240
	v_med3_i32 v156, v156, 31, v240
	v_med3_i32 v162, v162, 31, v240
	v_med3_i32 v168, v196, 31, v240
	v_add3_u32 v136, v244, v136, s59
	v_add3_u32 v137, v244, v137, s59
	v_add3_u32 v138, v244, v138, s59
	v_add3_u32 v139, v244, v139, s59
	v_add3_u32 v140, v244, v140, s59
	v_add3_u32 v141, v244, v141, s59
	v_add3_u32 v142, v244, v142, s59
	v_add3_u32 v143, v244, v143, s59
	v_add3_u32 v144, v244, v144, s59
	v_lshlrev_b32_e32 v145, 2, v145
	v_lshlrev_b32_e32 v146, 2, v146
	v_lshlrev_b32_e32 v147, 2, v147
	v_lshlrev_b32_e32 v153, 2, v153
	v_lshlrev_b32_e32 v156, 2, v156
	v_lshlrev_b32_e32 v162, 2, v162
	v_lshlrev_b32_e32 v168, 2, v168
	ds_read_b32 v136, v136
	ds_read_b32 v137, v137
	ds_read_b32 v138, v138
	ds_read_b32 v139, v139
	ds_read_b32 v140, v140
	ds_read_b32 v141, v141
	ds_read_b32 v142, v142
	ds_read_b32 v143, v143
	v_add3_u32 v145, v244, v145, s59
	v_add3_u32 v146, v244, v146, s59
	v_add3_u32 v147, v244, v147, s59
	v_add3_u32 v153, v244, v153, s59
	v_add3_u32 v156, v244, v156, s59
	v_add3_u32 v162, v244, v162, s59
	v_add3_u32 v168, v244, v168, s59
	ds_read_b32 v202, v144
	ds_read_b32 v201, v145
	ds_read_b32 v199, v146
	ds_read_b32 v200, v147
	ds_read_b32 v195, v153
	ds_read_b32 v194, v156
	ds_read_b32 v193, v162
	ds_read_b32 v192, v168
	v_add_u32_e32 v162, 3, v134
	v_add_u32_e32 v153, 5, v134
	v_add_u32_e32 v156, 7, v134
	s_waitcnt lgkmcnt(0)
	v_fmac_f32_e32 v137, 0x3e0293ee, v121
	v_sub_f32_e32 v121, v137, v4
	v_exp_f32_e32 v121, v121
	v_fmac_f32_e32 v136, 0x3e0293ee, v120
	v_fmac_f32_e32 v139, 0x3e0293ee, v123
	v_sub_f32_e32 v120, v136, v4
	v_mul_f32_e32 v136, v164, v121
	v_sub_f32_e32 v121, v139, v4
	v_exp_f32_e32 v121, v121
	v_cmp_le_i32_e32 vcc, v162, v172
	v_fmac_f32_e32 v141, 0x3e0293ee, v125
	v_fmac_f32_e32 v143, 0x3e0293ee, v127
	v_mul_f32_e32 v121, v164, v121
	v_cndmask_b32_e32 v190, 0, v121, vcc
	v_sub_f32_e32 v121, v141, v4
	v_exp_f32_e32 v123, v121
	v_fmac_f32_e32 v140, 0x3e0293ee, v124
	v_sub_f32_e32 v121, v140, v4
	v_exp_f32_e32 v120, v120
	v_mul_f32_e32 v137, v164, v123
	v_sub_f32_e32 v123, v143, v4
	v_exp_f32_e32 v124, v123
	v_exp_f32_e32 v121, v121
	v_fmac_f32_e32 v138, 0x3e0293ee, v122
	v_fmac_f32_e32 v142, 0x3e0293ee, v126
	v_sub_f32_e32 v122, v138, v4
	v_sub_f32_e32 v123, v142, v4
	v_exp_f32_e32 v122, v122
	v_exp_f32_e32 v123, v123
	v_mul_f32_e32 v124, v164, v124
	v_cmp_le_i32_e32 vcc, v156, v172
	v_pk_mul_f32 v[120:121], v[164:165], v[120:121]
	v_add_f32_dpp v142, v190, v190 quad_perm:[1,0,3,2] row_mask:0xf bank_mask:0xf bound_ctrl:1
	v_cndmask_b32_e32 v191, 0, v124, vcc
	v_cmp_le_i32_e32 vcc, v135, v167
	v_mov_b32_dpp v204, v142 quad_perm:[2,3,0,1] row_mask:0xf bank_mask:0xf bound_ctrl:1
	s_nop 0
	v_cndmask_b32_e32 v125, 0, v121, vcc
	v_cmp_le_i32_e32 vcc, v134, v172
	s_nop 1
	v_cndmask_b32_e32 v124, 0, v120, vcc
	v_cmp_ge_i32_e32 vcc, v172, v153
	v_pk_mul_f32 v[120:121], v[164:165], v[122:123]
	v_add_f32_dpp v123, v191, v191 quad_perm:[1,0,3,2] row_mask:0xf bank_mask:0xf bound_ctrl:1
	v_cndmask_b32_e32 v137, 0, v137, vcc
	v_cmp_lt_i32_e32 vcc, v134, v172
	v_add_f32_dpp v143, v123, v123 quad_perm:[2,3,0,1] row_mask:0xf bank_mask:0xf bound_ctrl:1
	ds_bpermute_b32 v203, v177, v143
	v_cndmask_b32_e32 v136, 0, v136, vcc
	v_cmp_le_i32_e32 vcc, v133, v167
	v_mov_b32_dpp v127, v137 quad_perm:[1,0,3,2] row_mask:0xf bank_mask:0xf bound_ctrl:1
	v_mov_b32_dpp v126, v136 quad_perm:[1,0,3,2] row_mask:0xf bank_mask:0xf bound_ctrl:1
	v_cndmask_b32_e32 v139, 0, v121, vcc
	v_cmp_le_i32_e32 vcc, v132, v172
	v_mov_b32_dpp v121, v125 quad_perm:[1,0,3,2] row_mask:0xf bank_mask:0xf bound_ctrl:1
	v_mov_b32_dpp v145, v139 quad_perm:[1,0,3,2] row_mask:0xf bank_mask:0xf bound_ctrl:1
	v_cndmask_b32_e32 v138, 0, v120, vcc
	v_mov_b32_dpp v120, v124 quad_perm:[1,0,3,2] row_mask:0xf bank_mask:0xf bound_ctrl:1
	v_pk_add_f32 v[120:121], v[124:125], v[120:121]
	v_mov_b32_dpp v144, v138 quad_perm:[1,0,3,2] row_mask:0xf bank_mask:0xf bound_ctrl:1
	v_pk_add_f32 v[126:127], v[136:137], v[126:127]
	v_pk_add_f32 v[144:145], v[138:139], v[144:145]
	v_mov_b32_dpp v122, v120 quad_perm:[2,3,0,1] row_mask:0xf bank_mask:0xf bound_ctrl:1
	v_mov_b32_dpp v140, v126 quad_perm:[2,3,0,1] row_mask:0xf bank_mask:0xf bound_ctrl:1
	v_mov_b32_dpp v146, v144 quad_perm:[2,3,0,1] row_mask:0xf bank_mask:0xf bound_ctrl:1
	v_mov_b32_dpp v123, v121 quad_perm:[2,3,0,1] row_mask:0xf bank_mask:0xf bound_ctrl:1
	v_mov_b32_dpp v141, v127 quad_perm:[2,3,0,1] row_mask:0xf bank_mask:0xf bound_ctrl:1
	v_mov_b32_dpp v147, v145 quad_perm:[2,3,0,1] row_mask:0xf bank_mask:0xf bound_ctrl:1
	s_and_saveexec_b64 s[6:7], s[4:5]
	s_cbranch_execz .LBB0_985
	v_pk_add_f32 v[126:127], v[126:127], v[140:141]
	v_pk_add_f32 v[120:121], v[120:121], v[122:123]
	v_pk_add_f32 v[144:145], v[144:145], v[146:147]
	v_pk_add_f32 v[120:121], v[120:121], v[126:127]
	s_waitcnt lgkmcnt(0)
	v_cndmask_b32_e64 v168, v203, v148, s[2:3]
	v_add_f32_e32 v169, v142, v204
	v_pk_add_f32 v[120:121], v[120:121], v[144:145]
	v_mov_b32_e32 v142, v169
	v_pk_fma_f32 v[120:121], v[120:121], 2.0, v[168:169] op_sel_hi:[1,0,1]
	v_add_u32_e32 v122, v236, v197
	v_pk_add_f32 v[120:121], v[142:143], v[120:121]
	ds_write_b64 v122, v[120:121]

.LBB0_990:
	s_add_i32 s35, s45, s50
	v_add_u32_e32 v50, s35, v152
	v_add_u32_e32 v51, s35, v151
	v_add_u32_e32 v144, s35, v150
	v_add_u32_e32 v145, s35, v149
	ds_read_b128 v[38:41], v50
	ds_read_b128 v[42:45], v50 offset:4096
	ds_read_b128 v[46:49], v51
	ds_read_b128 v[136:139], v51 offset:4096
	ds_read_b128 v[148:151], v144
	ds_read_b128 v[190:193], v144 offset:4096
	s_waitcnt lgkmcnt(0)
	ds_read_b128 v[200:203], v145
	ds_read_b128 v[204:207], v145 offset:4096
	s_setprio 1
	v_mfma_f32_16x16x32_f16 v[38:41], v[38:41], v[22:25], 0
	v_mfma_f32_16x16x32_f16 v[38:41], v[46:49], v[26:29], v[38:41]
	v_mfma_f32_16x16x32_f16 v[38:41], v[148:151], v[30:33], v[38:41]
	s_waitcnt lgkmcnt(0)
	v_mfma_f32_16x16x32_f16 v[46:49], v[200:203], v[34:37], v[38:41]
	v_mfma_f32_16x16x32_f16 v[38:41], v[42:45], v[22:25], 0
	v_mfma_f32_16x16x32_f16 v[38:41], v[136:139], v[26:29], v[38:41]
	v_mfma_f32_16x16x32_f16 v[38:41], v[190:193], v[30:33], v[38:41]
	v_mfma_f32_16x16x32_f16 v[136:139], v[204:207], v[34:37], v[38:41]
	s_setprio 0
	s_nop 5
	ds_read_b128 v[38:41], v50 offset:8192
	ds_read_b128 v[148:151], v50 offset:12288
	ds_read_b128 v[42:45], v51 offset:8192
	ds_read_b128 v[190:193], v51 offset:12288
	ds_read_b128 v[200:203], v144 offset:8192
	ds_read_b128 v[204:207], v144 offset:12288
	ds_read_b128 v[248:251], v145 offset:8192
	ds_read_b128 v[168:171], v145 offset:12288
	s_setprio 1
	s_waitcnt lgkmcnt(7)
	v_mfma_f32_16x16x32_f16 v[38:41], v[38:41], v[22:25], 0
	s_waitcnt lgkmcnt(5)
	v_mfma_f32_16x16x32_f16 v[38:41], v[42:45], v[26:29], v[38:41]
	s_waitcnt lgkmcnt(3)
	v_mfma_f32_16x16x32_f16 v[38:41], v[200:203], v[30:33], v[38:41]
	s_waitcnt lgkmcnt(1)
	v_mfma_f32_16x16x32_f16 v[42:45], v[248:251], v[34:37], v[38:41]
	v_mfma_f32_16x16x32_f16 v[38:41], v[148:151], v[22:25], 0
	v_mfma_f32_16x16x32_f16 v[38:41], v[190:193], v[26:29], v[38:41]
	v_mfma_f32_16x16x32_f16 v[38:41], v[204:207], v[30:33], v[38:41]
	s_waitcnt lgkmcnt(0)
	v_mfma_f32_16x16x32_f16 v[38:41], v[168:171], v[34:37], v[38:41]
	s_setprio 0
	v_add_u32_e32 v50, 0x274, v196
	v_add_u32_e32 v51, 0x264, v196
	v_sub_u32_e32 v144, v181, v154
	v_med3_i32 v50, v50, 31, v240
	v_med3_i32 v51, v51, 31, v240
	v_med3_i32 v144, v144, 31, v240
	v_sub_u32_e32 v143, v181, v143
	v_sub_u32_e32 v142, v181, v142
	v_sub_u32_e32 v141, v181, v141
	v_sub_u32_e32 v145, v181, v155
	v_sub_u32_e32 v140, v181, v140
	v_lshlrev_b32_e32 v50, 2, v50
	v_lshlrev_b32_e32 v51, 2, v51
	v_lshlrev_b32_e32 v144, 2, v144
	v_med3_i32 v143, v143, 31, v240
	v_med3_i32 v142, v142, 31, v240
	v_med3_i32 v141, v141, 31, v240
	v_med3_i32 v145, v145, 31, v240
	v_med3_i32 v140, v140, 31, v240
	v_add3_u32 v50, v244, v50, s59
	v_add3_u32 v51, v244, v51, s59
	v_add3_u32 v144, v244, v144, s59
	v_lshlrev_b32_e32 v143, 2, v143
	v_lshlrev_b32_e32 v142, 2, v142
	v_lshlrev_b32_e32 v141, 2, v141
	v_lshlrev_b32_e32 v145, 2, v145
	v_lshlrev_b32_e32 v140, 2, v140
	v_add3_u32 v143, v244, v143, s59
	v_add3_u32 v142, v244, v142, s59
	v_add3_u32 v141, v244, v141, s59
	v_add3_u32 v145, v244, v145, s59
	v_add3_u32 v140, v244, v140, s59
	ds_read_b32 v50, v50
	ds_read_b32 v51, v51
	ds_read_b32 v148, v144
	ds_read_b32 v151, v143
	ds_read_b32 v152, v142
	ds_read_b32 v154, v141
	ds_read_b32 v155, v145
	ds_read_b32 v158, v140
	v_sub_u32_e32 v144, v181, v187
	v_med3_i32 v144, v144, 31, v240
	v_sub_u32_e32 v140, v181, v157
	v_sub_u32_e32 v141, v181, v161
	v_sub_u32_e32 v142, v181, v163
	v_sub_u32_e32 v143, v181, v186
	v_lshlrev_b32_e32 v144, 2, v144
	v_med3_i32 v140, v140, 31, v240
	v_med3_i32 v141, v141, 31, v240
	v_med3_i32 v142, v142, 31, v240
	v_sub_u32_e32 v53, v181, v53
	v_med3_i32 v143, v143, 31, v240
	v_add3_u32 v157, v244, v144, s59
	v_sub_u32_e32 v144, v181, v189
	v_sub_u32_e32 v52, v181, v52
	v_lshlrev_b32_e32 v140, 2, v140
	v_lshlrev_b32_e32 v141, 2, v141
	v_lshlrev_b32_e32 v142, 2, v142
	v_med3_i32 v53, v53, 31, v240
	v_lshlrev_b32_e32 v143, 2, v143
	v_med3_i32 v144, v144, 31, v240
	v_med3_i32 v52, v52, 31, v240
	v_add3_u32 v140, v244, v140, s59
	v_add3_u32 v141, v244, v141, s59
	v_add3_u32 v142, v244, v142, s59
	v_lshlrev_b32_e32 v53, 2, v53
	v_add3_u32 v143, v244, v143, s59
	v_lshlrev_b32_e32 v144, 2, v144
	v_lshlrev_b32_e32 v52, 2, v52
	v_add3_u32 v53, v244, v53, s59
	v_add3_u32 v159, v244, v144, s59
	v_add3_u32 v52, v244, v52, s59
	ds_read_b32 v150, v140
	ds_read_b32 v149, v141
	ds_read_b32 v144, v142
	ds_read_b32 v145, v53
	ds_read_b32 v143, v143
	ds_read_b32 v142, v157
	ds_read_b32 v141, v159
	ds_read_b32 v140, v52
	s_waitcnt lgkmcnt(0)
	v_fmac_f32_e32 v51, 0x3e0293ee, v47
	v_sub_f32_e32 v47, v51, v5
	v_exp_f32_e32 v47, v47
	v_fmac_f32_e32 v50, 0x3e0293ee, v46
	v_fmac_f32_e32 v151, 0x3e0293ee, v49
	v_sub_f32_e32 v46, v50, v5
	v_mul_f32_e32 v50, v182, v47
	v_sub_f32_e32 v47, v151, v5
	v_exp_f32_e32 v47, v47
	v_cmp_le_i32_e32 vcc, v162, v184
	v_fmac_f32_e32 v154, 0x3e0293ee, v137
	v_fmac_f32_e32 v158, 0x3e0293ee, v139
	v_mul_f32_e32 v47, v182, v47
	v_cndmask_b32_e32 v200, 0, v47, vcc
	v_sub_f32_e32 v47, v154, v5
	v_exp_f32_e32 v49, v47
	v_fmac_f32_e32 v152, 0x3e0293ee, v136
	v_sub_f32_e32 v47, v152, v5
	v_exp_f32_e32 v46, v46
	v_mul_f32_e32 v51, v182, v49
	v_sub_f32_e32 v49, v158, v5
	v_exp_f32_e32 v52, v49
	v_exp_f32_e32 v47, v47
	v_fmac_f32_e32 v148, 0x3e0293ee, v48
	v_fmac_f32_e32 v155, 0x3e0293ee, v138
	v_sub_f32_e32 v48, v148, v5
	v_sub_f32_e32 v49, v155, v5
	v_mul_f32_e32 v52, v182, v52
	v_cmp_le_i32_e32 vcc, v156, v184
	v_exp_f32_e32 v48, v48
	v_exp_f32_e32 v49, v49
	v_cndmask_b32_e32 v201, 0, v52, vcc
	v_pk_mul_f32 v[46:47], v[182:183], v[46:47]
	v_cmp_le_i32_e32 vcc, v135, v1
	v_pk_mul_f32 v[48:49], v[182:183], v[48:49]
	v_add_f32_dpp v152, v200, v200 quad_perm:[1,0,3,2] row_mask:0xf bank_mask:0xf bound_ctrl:1
	v_cndmask_b32_e32 v47, 0, v47, vcc
	v_cmp_le_i32_e32 vcc, v134, v184
	v_mov_b32_dpp v154, v152 quad_perm:[2,3,0,1] row_mask:0xf bank_mask:0xf bound_ctrl:1
	v_add_u32_e32 v148, v236, v197
	v_cndmask_b32_e32 v46, 0, v46, vcc
	v_cmp_ge_i32_e32 vcc, v184, v153
	s_nop 1
	v_cndmask_b32_e32 v187, 0, v51, vcc
	v_cmp_lt_i32_e32 vcc, v134, v184
	v_add_f32_dpp v51, v201, v201 quad_perm:[1,0,3,2] row_mask:0xf bank_mask:0xf bound_ctrl:1
	v_mov_b32_dpp v53, v187 quad_perm:[1,0,3,2] row_mask:0xf bank_mask:0xf bound_ctrl:1
	v_cndmask_b32_e32 v186, 0, v50, vcc
	v_cmp_le_i32_e32 vcc, v133, v1
	s_nop 0
	v_mov_b32_dpp v52, v186 quad_perm:[1,0,3,2] row_mask:0xf bank_mask:0xf bound_ctrl:1
	v_cndmask_b32_e32 v189, 0, v49, vcc
	v_cmp_le_i32_e32 vcc, v132, v184
	v_mov_b32_dpp v49, v47 quad_perm:[1,0,3,2] row_mask:0xf bank_mask:0xf bound_ctrl:1
	v_mov_b32_dpp v135, v189 quad_perm:[1,0,3,2] row_mask:0xf bank_mask:0xf bound_ctrl:1
	v_cndmask_b32_e32 v188, 0, v48, vcc
	v_mov_b32_dpp v48, v46 quad_perm:[1,0,3,2] row_mask:0xf bank_mask:0xf bound_ctrl:1
	v_pk_add_f32 v[48:49], v[46:47], v[48:49]
	v_mov_b32_dpp v134, v188 quad_perm:[1,0,3,2] row_mask:0xf bank_mask:0xf bound_ctrl:1
	v_pk_add_f32 v[136:137], v[188:189], v[134:135]
	v_add_f32_dpp v135, v51, v51 quad_perm:[2,3,0,1] row_mask:0xf bank_mask:0xf bound_ctrl:1
	ds_bpermute_b32 v151, v177, v135
	v_pk_add_f32 v[52:53], v[186:187], v[52:53]
	v_mov_b32_dpp v50, v48 quad_perm:[2,3,0,1] row_mask:0xf bank_mask:0xf bound_ctrl:1
	v_mov_b32_dpp v138, v136 quad_perm:[2,3,0,1] row_mask:0xf bank_mask:0xf bound_ctrl:1
	v_mov_b32_dpp v132, v52 quad_perm:[2,3,0,1] row_mask:0xf bank_mask:0xf bound_ctrl:1
	v_mov_b32_dpp v51, v49 quad_perm:[2,3,0,1] row_mask:0xf bank_mask:0xf bound_ctrl:1
	v_mov_b32_dpp v133, v53 quad_perm:[2,3,0,1] row_mask:0xf bank_mask:0xf bound_ctrl:1
	v_mov_b32_dpp v139, v137 quad_perm:[2,3,0,1] row_mask:0xf bank_mask:0xf bound_ctrl:1
	s_and_saveexec_b64 s[6:7], s[4:5]
	s_cbranch_execz .LBB0_992
	v_pk_add_f32 v[52:53], v[52:53], v[132:133]
	v_pk_add_f32 v[48:49], v[48:49], v[50:51]
	v_pk_add_f32 v[136:137], v[136:137], v[138:139]
	v_pk_add_f32 v[48:49], v[48:49], v[52:53]
	s_waitcnt lgkmcnt(0)
	v_cndmask_b32_e64 v156, v151, v118, s[2:3]
	v_add_f32_e32 v157, v152, v154
	v_pk_add_f32 v[48:49], v[48:49], v[136:137]
	v_mov_b32_e32 v134, v157
	v_pk_fma_f32 v[48:49], v[48:49], 2.0, v[156:157] op_sel_hi:[1,0,1]
	s_nop 0
	v_pk_add_f32 v[48:49], v[134:135], v[48:49]
	ds_write_b64 v148, v[48:49] offset:2048

.LBB0_1133:
	s_waitcnt lgkmcnt(0)
	s_sub_i32 s6, s96, 64
	s_lshr_b64 s[18:19], s[26:27], s96
	s_lshr_b64 s[20:21], s[28:29], s6
	s_lshr_b64 s[34:35], s[22:23], s96
	s_lshr_b64 s[38:39], s[24:25], s6
	s_cmp_lt_u32 s96, 64
	s_cselect_b64 s[0:1], -1, 0
	s_and_b64 s[42:43], s[0:1], exec
	s_cselect_b32 s7, s18, s20
	s_cselect_b32 s20, s34, s38
	s_bitcmp1_b32 s7, 0
	s_cselect_b64 s[18:19], -1, 0
	s_bitcmp1_b32 s20, 0
	s_cselect_b64 s[76:77], -1, 0
	s_or_b64 s[20:21], s[18:19], s[76:77]
	s_andn2_b64 vcc, exec, s[20:21]
	s_cbranch_vccnz .LBB0_1139
	v_lshrrev_b64 v[118:119], s96, v[200:201]
	v_lshrrev_b64 v[120:121], s6, v[202:203]
	v_cndmask_b32_e64 v2, v120, v118, s[0:1]
	v_lshrrev_b64 v[118:119], s96, v[196:197]
	v_lshrrev_b64 v[120:121], s6, v[198:199]
	v_cndmask_b32_e64 v1, v120, v118, s[0:1]
	s_mul_hi_u32 s0, s50, 0xaaaaaaab
	s_lshr_b32 s34, s0, 1
	s_and_b64 s[6:7], s[18:19], s[76:77]
	s_cmpk_lt_i32 s45, 0x7f
	s_cselect_b64 s[0:1], -1, 0
	s_cmpk_gt_i32 s45, 0x7e
	s_cselect_b64 s[20:21], -1, 0
	s_mul_i32 s34, s34, 0x18000
	s_and_b64 s[20:21], s[20:21], s[6:7]
	v_cndmask_b32_e64 v5, 0, 1, s[18:19]
	v_subrev_u32_e32 v142, s34, v232
	v_subrev_u32_e32 v143, s34, v233
	v_subrev_u32_e32 v144, s34, v234
	v_subrev_u32_e32 v145, s34, v235
	s_mov_b64 s[6:7], -1
	s_andn2_b64 vcc, exec, s[20:21]
	v_cmp_ne_u32_e64 s[18:19], 1, v5
	s_cbranch_vccz .LBB0_1160
	s_and_b64 vcc, exec, s[18:19]
	v_mov_b64_e32 v[204:205], v[136:137]
	v_mov_b64_e32 v[206:207], v[134:135]
	s_cbranch_vccnz .LBB0_1147
	s_add_i32 s6, s9, s8
	v_add_u32_e32 v5, s6, v145
	v_add_u32_e32 v150, s6, v144
	v_add_u32_e32 v151, s6, v143
	v_add_u32_e32 v154, s6, v142
	ds_read_b128 v[38:41], v5
	ds_read_b128 v[42:45], v5 offset:4096
	ds_read_b128 v[118:121], v150
	ds_read_b128 v[122:125], v150 offset:4096
	ds_read_b128 v[126:129], v151
	ds_read_b128 v[138:141], v151 offset:4096
	ds_read_b128 v[130:133], v154
	ds_read_b128 v[146:149], v154 offset:4096
	s_setprio 1
	s_waitcnt lgkmcnt(7)
	v_mfma_f32_16x16x32_f16 v[38:41], v[38:41], v[6:9], 0
	s_waitcnt lgkmcnt(5)
	v_mfma_f32_16x16x32_f16 v[38:41], v[118:121], v[10:13], v[38:41]
	s_waitcnt lgkmcnt(3)
	v_mfma_f32_16x16x32_f16 v[38:41], v[126:129], v[14:17], v[38:41]
	s_waitcnt lgkmcnt(1)
	v_mfma_f32_16x16x32_f16 v[130:133], v[130:133], v[18:21], v[38:41]
	v_mfma_f32_16x16x32_f16 v[38:41], v[42:45], v[6:9], 0
	v_mfma_f32_16x16x32_f16 v[38:41], v[122:125], v[10:13], v[38:41]
	v_mfma_f32_16x16x32_f16 v[38:41], v[138:141], v[14:17], v[38:41]
	s_waitcnt lgkmcnt(0)
	v_mfma_f32_16x16x32_f16 v[126:129], v[146:149], v[18:21], v[38:41]
	s_setprio 0
	s_nop 5
	ds_read_b128 v[38:41], v5 offset:8192
	ds_read_b128 v[42:45], v5 offset:12288
	ds_read_b128 v[118:121], v150 offset:8192
	ds_read_b128 v[138:141], v150 offset:12288
	ds_read_b128 v[122:125], v151 offset:8192
	ds_read_b128 v[146:149], v151 offset:12288
	ds_read_b128 v[150:153], v154 offset:8192
	ds_read_b128 v[154:157], v154 offset:12288
	s_setprio 1
	s_waitcnt lgkmcnt(7)
	v_mfma_f32_16x16x32_f16 v[38:41], v[38:41], v[6:9], 0
	s_waitcnt lgkmcnt(5)
	v_mfma_f32_16x16x32_f16 v[38:41], v[118:121], v[10:13], v[38:41]
	s_waitcnt lgkmcnt(3)
	v_mfma_f32_16x16x32_f16 v[38:41], v[122:125], v[14:17], v[38:41]
	s_waitcnt lgkmcnt(1)
	v_mfma_f32_16x16x32_f16 v[122:125], v[150:153], v[18:21], v[38:41]
	v_mfma_f32_16x16x32_f16 v[38:41], v[42:45], v[6:9], 0
	v_mfma_f32_16x16x32_f16 v[38:41], v[138:141], v[10:13], v[38:41]
	v_mfma_f32_16x16x32_f16 v[38:41], v[146:149], v[14:17], v[38:41]
	s_waitcnt lgkmcnt(0)
	v_mfma_f32_16x16x32_f16 v[118:121], v[154:157], v[18:21], v[38:41]
	s_setprio 0
	s_mov_b64 s[6:7], -1
	s_and_b64 vcc, exec, s[0:1]
	s_cbranch_vccz .LBB0_1142
	v_add_u32_e32 v5, s45, v238
	s_nop 1
	v_add_u32_e32 v38, 63, v5
	v_add_u32_e32 v40, 62, v5
	v_add_u32_e32 v42, 61, v5
	v_add_u32_e32 v44, 60, v5
	v_add_u32_e32 v138, 59, v5
	v_add_u32_e32 v140, 58, v5
	v_add_u32_e32 v146, 57, v5
	v_add_u32_e32 v148, 56, v5
	v_add_u32_e32 v150, 31, v5
	v_add_u32_e32 v152, 30, v5
	v_add_u32_e32 v154, 29, v5
	v_add_u32_e32 v156, 28, v5
	v_add_u32_e32 v158, 27, v5
	v_add_u32_e32 v160, 26, v5
	v_add_u32_e32 v162, 25, v5
	v_med3_i32 v39, v38, 0, v243
	v_med3_i32 v41, v40, 0, v243
	v_med3_i32 v43, v42, 0, v243
	v_med3_i32 v45, v44, 0, v243
	v_med3_i32 v139, v138, 0, v243
	v_med3_i32 v141, v140, 0, v243
	v_med3_i32 v147, v146, 0, v243
	v_med3_i32 v149, v148, 0, v243
	v_med3_i32 v151, v150, 0, v243
	v_med3_i32 v153, v152, 0, v243
	v_med3_i32 v155, v154, 0, v243
	v_med3_i32 v157, v156, 0, v243
	v_med3_i32 v159, v158, 0, v243
	v_med3_i32 v161, v160, 0, v243
	v_med3_i32 v163, v162, 0, v243
	v_add_u32_e32 v164, 24, v5
	v_lshl_add_u32 v39, v39, 2, v244
	v_lshl_add_u32 v41, v41, 2, v244
	v_lshl_add_u32 v43, v43, 2, v244
	v_lshl_add_u32 v45, v45, 2, v244
	v_lshl_add_u32 v139, v139, 2, v244
	v_lshl_add_u32 v141, v141, 2, v244
	v_lshl_add_u32 v147, v147, 2, v244
	v_lshl_add_u32 v149, v149, 2, v244
	v_lshl_add_u32 v151, v151, 2, v244
	v_lshl_add_u32 v153, v153, 2, v244
	v_lshl_add_u32 v155, v155, 2, v244
	v_lshl_add_u32 v157, v157, 2, v244
	v_lshl_add_u32 v159, v159, 2, v244
	v_lshl_add_u32 v161, v161, 2, v244
	v_lshl_add_u32 v163, v163, 2, v244
	v_med3_i32 v5, v164, 0, v243
	ds_read_b32 v39, v39
	ds_read_b32 v41, v41
	ds_read_b32 v43, v43
	ds_read_b32 v45, v45
	ds_read_b32 v139, v139
	ds_read_b32 v141, v141
	ds_read_b32 v147, v147
	ds_read_b32 v149, v149
	v_lshl_add_u32 v5, v5, 2, v244
	ds_read_b32 v151, v151
	ds_read_b32 v153, v153
	ds_read_b32 v155, v155
	ds_read_b32 v157, v157
	ds_read_b32 v159, v159
	ds_read_b32 v161, v161
	ds_read_b32 v163, v163
	ds_read_b32 v165, v5
	v_and_b32_e32 v5, 1, v2
	v_cmp_eq_u32_e32 vcc, 1, v5
	v_cmp_lt_i32_e64 s[0:1], -1, v38
	s_waitcnt lgkmcnt(0)
	v_fmac_f32_e32 v39, 0x3e0293ee, v130
	s_and_b64 s[0:1], s[0:1], vcc
	v_cndmask_b32_e64 v5, v241, v39, s[0:1]
	v_cmp_lt_i32_e64 s[0:1], -1, v40
	v_fmac_f32_e32 v41, 0x3e0293ee, v131
	s_and_b64 s[0:1], s[0:1], vcc
	v_cndmask_b32_e64 v38, v241, v41, s[0:1]
	v_cmp_lt_i32_e64 s[0:1], -1, v42
	v_fmac_f32_e32 v43, 0x3e0293ee, v132
	s_and_b64 s[0:1], s[0:1], vcc
	v_cndmask_b32_e64 v39, v241, v43, s[0:1]
	v_cmp_lt_i32_e64 s[0:1], -1, v44
	v_fmac_f32_e32 v45, 0x3e0293ee, v133
	s_and_b64 s[0:1], s[0:1], vcc
	v_cndmask_b32_e64 v41, v241, v45, s[0:1]
	v_cmp_lt_i32_e64 s[0:1], -1, v138
	v_fmac_f32_e32 v139, 0x3e0293ee, v126
	s_and_b64 s[0:1], s[0:1], vcc
	v_cndmask_b32_e64 v40, v241, v139, s[0:1]
	v_cmp_lt_i32_e64 s[0:1], -1, v140
	v_fmac_f32_e32 v141, 0x3e0293ee, v127
	s_and_b64 s[0:1], s[0:1], vcc
	v_cndmask_b32_e64 v140, v241, v141, s[0:1]
	v_cmp_lt_i32_e64 s[0:1], -1, v146
	v_fmac_f32_e32 v147, 0x3e0293ee, v128
	s_and_b64 s[0:1], s[0:1], vcc
	v_cndmask_b32_e64 v147, v241, v147, s[0:1]
	v_cmp_lt_i32_e64 s[0:1], -1, v148
	v_fmac_f32_e32 v149, 0x3e0293ee, v129
	s_and_b64 s[0:1], s[0:1], vcc
	v_cndmask_b32_e64 v149, v241, v149, s[0:1]
	v_cmp_lt_i32_e64 s[0:1], -1, v150
	v_fmac_f32_e32 v151, 0x3e0293ee, v122
	s_and_b64 s[0:1], s[0:1], vcc
	v_cndmask_b32_e64 v44, v241, v151, s[0:1]
	v_cmp_lt_i32_e64 s[0:1], -1, v152
	v_fmac_f32_e32 v153, 0x3e0293ee, v123
	s_and_b64 s[0:1], s[0:1], vcc
	v_cndmask_b32_e64 v45, v241, v153, s[0:1]
	v_cmp_lt_i32_e64 s[0:1], -1, v154
	v_fmac_f32_e32 v155, 0x3e0293ee, v124
	s_and_b64 s[0:1], s[0:1], vcc
	v_cndmask_b32_e64 v138, v241, v155, s[0:1]
	v_cmp_lt_i32_e64 s[0:1], -1, v156
	v_fmac_f32_e32 v157, 0x3e0293ee, v125
	s_and_b64 s[0:1], s[0:1], vcc
	v_cndmask_b32_e64 v141, v241, v157, s[0:1]
	v_cmp_lt_i32_e64 s[0:1], -1, v158
	v_fmac_f32_e32 v159, 0x3e0293ee, v118
	s_and_b64 s[0:1], s[0:1], vcc
	v_cndmask_b32_e64 v139, v241, v159, s[0:1]
	v_cmp_lt_i32_e64 s[0:1], -1, v160
	v_max_f32_e32 v42, v5, v38
	v_fmac_f32_e32 v161, 0x3e0293ee, v119
	s_and_b64 s[0:1], s[0:1], vcc
	v_max3_f32 v42, v42, v39, v41
	v_cndmask_b32_e64 v146, v241, v161, s[0:1]
	v_cmp_lt_i32_e64 s[0:1], -1, v162
	v_max3_f32 v42, v42, v40, v140
	v_fmac_f32_e32 v163, 0x3e0293ee, v120
	s_and_b64 s[0:1], s[0:1], vcc
	v_max3_f32 v42, v42, v147, v149
	v_cndmask_b32_e64 v148, v241, v163, s[0:1]
	v_cmp_lt_i32_e64 s[0:1], -1, v164
	v_max3_f32 v42, v42, v44, v45
	v_fmac_f32_e32 v165, 0x3e0293ee, v121
	s_and_b64 vcc, s[0:1], vcc
	v_max3_f32 v42, v42, v138, v141
	v_cndmask_b32_e32 v150, v241, v165, vcc
	v_max3_f32 v42, v42, v139, v146
	v_max3_f32 v42, v42, v148, v150
	v_add_f32_e32 v43, 0x41000000, v136
	v_cmp_gt_f32_e32 vcc, v42, v43
	s_cbranch_vccz .LBB0_1140
	ds_bpermute_b32 v43, v245, v42
	v_max_f32_e32 v42, v42, v42
	s_waitcnt lgkmcnt(0)
	v_max_f32_e32 v43, v43, v43
	v_max_f32_e32 v42, v42, v43
	ds_bpermute_b32 v43, v246, v42
	s_waitcnt lgkmcnt(0)
	v_max3_f32 v42, v136, v42, v43
	v_sub_f32_e32 v43, v136, v42
	v_exp_f32_e32 v194, v43
	v_mov_b32_e32 v43, v137
	v_mov_b64_e32 v[204:205], v[42:43]
	s_branch .LBB0_1141

.LBB0_1147:
	s_andn2_b64 vcc, exec, s[76:77]
	s_cbranch_vccnz .LBB0_1159
	s_add_i32 s0, s9, s8
	v_add_u32_e32 v4, s0, v145
	v_add_u32_e32 v5, s0, v144
	v_add_u32_e32 v150, s0, v143
	v_add_u32_e32 v154, s0, v142
	ds_read_b128 v[46:49], v4
	ds_read_b128 v[50:53], v4 offset:4096
	ds_read_b128 v[118:121], v5
	ds_read_b128 v[122:125], v5 offset:4096
	ds_read_b128 v[126:129], v150
	ds_read_b128 v[138:141], v150 offset:4096
	ds_read_b128 v[130:133], v154
	ds_read_b128 v[146:149], v154 offset:4096
	s_setprio 1
	s_waitcnt lgkmcnt(7)
	v_mfma_f32_16x16x32_f16 v[46:49], v[46:49], v[22:25], 0
	s_waitcnt lgkmcnt(5)
	v_mfma_f32_16x16x32_f16 v[46:49], v[118:121], v[26:29], v[46:49]
	s_waitcnt lgkmcnt(3)
	v_mfma_f32_16x16x32_f16 v[46:49], v[126:129], v[30:33], v[46:49]
	s_waitcnt lgkmcnt(1)
	v_mfma_f32_16x16x32_f16 v[130:133], v[130:133], v[34:37], v[46:49]
	v_mfma_f32_16x16x32_f16 v[46:49], v[50:53], v[22:25], 0
	v_mfma_f32_16x16x32_f16 v[46:49], v[122:125], v[26:29], v[46:49]
	v_mfma_f32_16x16x32_f16 v[46:49], v[138:141], v[30:33], v[46:49]
	s_waitcnt lgkmcnt(0)
	v_mfma_f32_16x16x32_f16 v[126:129], v[146:149], v[34:37], v[46:49]
	s_setprio 0
	s_nop 5
	ds_read_b128 v[46:49], v4 offset:8192
	ds_read_b128 v[50:53], v4 offset:12288
	ds_read_b128 v[118:121], v5 offset:8192
	ds_read_b128 v[138:141], v5 offset:12288
	ds_read_b128 v[122:125], v150 offset:8192
	ds_read_b128 v[146:149], v150 offset:12288
	ds_read_b128 v[150:153], v154 offset:8192
	ds_read_b128 v[154:157], v154 offset:12288
	s_setprio 1
	s_waitcnt lgkmcnt(7)
	v_mfma_f32_16x16x32_f16 v[46:49], v[46:49], v[22:25], 0
	s_waitcnt lgkmcnt(5)
	v_mfma_f32_16x16x32_f16 v[46:49], v[118:121], v[26:29], v[46:49]
	s_waitcnt lgkmcnt(3)
	v_mfma_f32_16x16x32_f16 v[46:49], v[122:125], v[30:33], v[46:49]
	s_waitcnt lgkmcnt(1)
	v_mfma_f32_16x16x32_f16 v[122:125], v[150:153], v[34:37], v[46:49]
	v_mfma_f32_16x16x32_f16 v[46:49], v[50:53], v[22:25], 0
	v_mfma_f32_16x16x32_f16 v[46:49], v[138:141], v[26:29], v[46:49]
	v_mfma_f32_16x16x32_f16 v[46:49], v[146:149], v[30:33], v[46:49]
	s_waitcnt lgkmcnt(0)
	v_mfma_f32_16x16x32_f16 v[118:121], v[154:157], v[34:37], v[46:49]
	s_setprio 0
	s_add_i32 s0, s45, 4
	s_cmpk_gt_i32 s0, 0x7e
	s_mov_b64 s[0:1], -1
	s_cbranch_scc1 .LBB0_1153
	v_add_u32_e32 v4, s45, v238
	s_nop 0
	v_add_u32_e32 v48, 0x43, v4
	v_max_i32_e32 v46, 1, v48
	v_max_i32_e32 v47, 2, v48
	v_max_i32_e32 v49, 3, v48
	v_max_i32_e32 v50, 4, v48
	v_add_u32_e32 v46, -1, v46
	v_add_u32_e32 v47, -2, v47
	v_add_u32_e32 v49, -3, v49
	v_add_u32_e32 v50, -4, v50
	v_add_u32_e32 v51, 62, v4
	v_add_u32_e32 v53, 61, v4
	v_add_u32_e32 v139, 60, v4
	v_add_u32_e32 v141, 35, v4
	v_add_u32_e32 v147, 34, v4
	v_add_u32_e32 v150, 33, v4
	v_add_u32_e32 v152, 32, v4
	v_add_u32_e32 v153, 31, v4
	v_add_u32_e32 v155, 30, v4
	v_add_u32_e32 v157, 29, v4
	v_add_u32_e32 v4, 28, v4
	v_med3_i32 v5, v48, 0, v243
	v_min_u32_e32 v46, 0x7f, v46
	v_min_u32_e32 v47, 0x7f, v47
	v_min_u32_e32 v49, 0x7f, v49
	v_min_u32_e32 v50, 0x7f, v50
	v_med3_i32 v52, v51, 0, v243
	v_med3_i32 v138, v53, 0, v243
	v_med3_i32 v140, v139, 0, v243
	v_med3_i32 v146, v141, 0, v243
	v_med3_i32 v148, v147, 0, v243
	v_med3_i32 v154, v153, 0, v243
	v_med3_i32 v156, v155, 0, v243
	v_med3_i32 v158, v157, 0, v243
	v_med3_i32 v159, v4, 0, v243
	v_lshl_add_u32 v5, v5, 2, v244
	v_lshl_add_u32 v46, v46, 2, v244
	v_lshl_add_u32 v47, v47, 2, v244
	v_lshl_add_u32 v49, v49, 2, v244
	v_lshl_add_u32 v50, v50, 2, v244
	v_lshl_add_u32 v52, v52, 2, v244
	v_lshl_add_u32 v138, v138, 2, v244
	v_lshl_add_u32 v140, v140, 2, v244
	v_lshl_add_u32 v146, v146, 2, v244
	v_lshl_add_u32 v148, v148, 2, v244
	v_med3_i32 v149, v150, 0, v243
	v_med3_i32 v151, v152, 0, v243
	v_lshl_add_u32 v154, v154, 2, v244
	v_lshl_add_u32 v156, v156, 2, v244
	v_lshl_add_u32 v158, v158, 2, v244
	v_lshl_add_u32 v159, v159, 2, v244
	ds_read_b32 v5, v5
	ds_read_b32 v46, v46
	ds_read_b32 v47, v47
	ds_read_b32 v49, v49
	ds_read_b32 v50, v50
	ds_read_b32 v52, v52
	ds_read_b32 v138, v138
	ds_read_b32 v140, v140
	v_lshl_add_u32 v149, v149, 2, v244
	v_lshl_add_u32 v151, v151, 2, v244
	ds_read_b32 v160, v146
	ds_read_b32 v148, v148
	ds_read_b32 v161, v149
	ds_read_b32 v162, v151
	ds_read_b32 v154, v154
	ds_read_b32 v156, v156
	ds_read_b32 v158, v158
	ds_read_b32 v159, v159
	v_and_b32_e32 v146, 1, v1
	v_cmp_eq_u32_e32 vcc, 1, v146
	v_cmp_lt_i32_e64 s[0:1], -1, v48
	s_waitcnt lgkmcnt(0)
	v_fmac_f32_e32 v5, 0x3e0293ee, v130
	s_and_b64 s[0:1], s[0:1], vcc
	v_cndmask_b32_e64 v5, v241, v5, s[0:1]
	v_cmp_lt_i32_e64 s[0:1], 0, v48
	v_fmac_f32_e32 v46, 0x3e0293ee, v131
	s_and_b64 s[0:1], s[0:1], vcc
	v_cndmask_b32_e64 v46, v241, v46, s[0:1]
	v_cmp_lt_i32_e64 s[0:1], 1, v48
	v_fmac_f32_e32 v47, 0x3e0293ee, v132
	s_and_b64 s[0:1], s[0:1], vcc
	v_cndmask_b32_e64 v47, v241, v47, s[0:1]
	v_cmp_lt_i32_e64 s[0:1], 2, v48
	v_fmac_f32_e32 v49, 0x3e0293ee, v133
	s_and_b64 s[0:1], s[0:1], vcc
	v_cndmask_b32_e64 v49, v241, v49, s[0:1]
	v_cmp_lt_i32_e64 s[0:1], 3, v48
	v_fmac_f32_e32 v50, 0x3e0293ee, v126
	s_and_b64 s[0:1], s[0:1], vcc
	v_cndmask_b32_e64 v48, v241, v50, s[0:1]
	v_cmp_lt_i32_e64 s[0:1], -1, v51
	v_fmac_f32_e32 v52, 0x3e0293ee, v127
	s_and_b64 s[0:1], s[0:1], vcc
	v_cndmask_b32_e64 v146, v241, v52, s[0:1]
	v_cmp_lt_i32_e64 s[0:1], -1, v53
	v_fmac_f32_e32 v138, 0x3e0293ee, v128
	s_and_b64 s[0:1], s[0:1], vcc
	v_cndmask_b32_e64 v149, v241, v138, s[0:1]
	v_cmp_lt_i32_e64 s[0:1], -1, v139
	v_fmac_f32_e32 v140, 0x3e0293ee, v129
	s_and_b64 s[0:1], s[0:1], vcc
	v_cndmask_b32_e64 v151, v241, v140, s[0:1]
	v_cmp_lt_i32_e64 s[0:1], -1, v141
	v_fmac_f32_e32 v160, 0x3e0293ee, v122
	s_and_b64 s[0:1], s[0:1], vcc
	v_cndmask_b32_e64 v52, v241, v160, s[0:1]
	v_cmp_lt_i32_e64 s[0:1], -1, v147
	v_fmac_f32_e32 v148, 0x3e0293ee, v123
	s_and_b64 s[0:1], s[0:1], vcc
	v_cndmask_b32_e64 v53, v241, v148, s[0:1]
	v_cmp_lt_i32_e64 s[0:1], -1, v150
	v_fmac_f32_e32 v161, 0x3e0293ee, v124
	s_and_b64 s[0:1], s[0:1], vcc
	v_cndmask_b32_e64 v140, v241, v161, s[0:1]
	v_cmp_lt_i32_e64 s[0:1], -1, v152
	v_fmac_f32_e32 v162, 0x3e0293ee, v125
	s_and_b64 s[0:1], s[0:1], vcc
	v_cndmask_b32_e64 v147, v241, v162, s[0:1]
	v_cmp_lt_i32_e64 s[0:1], -1, v153
	v_fmac_f32_e32 v154, 0x3e0293ee, v118
	s_and_b64 s[0:1], s[0:1], vcc
	v_cndmask_b32_e64 v141, v241, v154, s[0:1]
	v_cmp_lt_i32_e64 s[0:1], -1, v155
	v_fmac_f32_e32 v156, 0x3e0293ee, v119
	s_and_b64 s[0:1], s[0:1], vcc
	v_cndmask_b32_e64 v148, v241, v156, s[0:1]
	v_cmp_lt_i32_e64 s[0:1], -1, v157
	v_fmac_f32_e32 v158, 0x3e0293ee, v120
	s_and_b64 s[0:1], s[0:1], vcc
	v_cndmask_b32_e64 v150, v241, v158, s[0:1]
	v_cmp_lt_i32_e64 s[0:1], -1, v4
	v_max_f32_e32 v4, v5, v46
	v_max3_f32 v4, v4, v47, v49
	v_max3_f32 v4, v4, v48, v146
	v_max3_f32 v4, v4, v149, v151
	v_max3_f32 v4, v4, v52, v53
	v_fmac_f32_e32 v159, 0x3e0293ee, v121
	s_and_b64 vcc, s[0:1], vcc
	v_max3_f32 v4, v4, v140, v147
	v_cndmask_b32_e32 v152, v241, v159, vcc
	v_max3_f32 v4, v4, v141, v148
	v_max3_f32 v4, v4, v150, v152
	v_add_f32_e32 v50, 0x41000000, v205
	v_cmp_gt_f32_e32 vcc, v4, v50
	s_cbranch_vccz .LBB0_1151
	ds_bpermute_b32 v50, v245, v4
	v_max_f32_e32 v4, v4, v4
	s_waitcnt lgkmcnt(0)
	v_max_f32_e32 v50, v50, v50
	v_max_f32_e32 v4, v4, v50
	ds_bpermute_b32 v50, v246, v4
	s_waitcnt lgkmcnt(0)
	v_max3_f32 v51, v205, v4, v50
	v_sub_f32_e32 v4, v205, v51
	v_exp_f32_e32 v4, v4
	v_mov_b32_e32 v50, v204
	v_mov_b64_e32 v[138:139], v[50:51]
	s_branch .LBB0_1152

.LBB0_1203:
	s_waitcnt lgkmcnt(0)
	s_add_i32 s34, s10, 63
	s_cmp_le_i32 s10, s9
	s_cselect_b64 s[6:7], -1, 0
	s_cmp_ge_i32 s34, s17
	s_cselect_b64 s[18:19], -1, 0
	s_and_b64 s[18:19], s[6:7], s[18:19]
	s_cmp_le_i32 s10, s8
	s_cselect_b64 s[20:21], -1, 0
	s_cmp_ge_i32 s34, s44
	s_cselect_b64 s[6:7], -1, 0
	s_and_b64 s[36:37], s[20:21], s[6:7]
	s_or_b64 s[20:21], s[18:19], s[36:37]
	s_andn2_b64 vcc, exec, s[20:21]
	s_cbranch_vccnz .LBB0_1209
	s_mul_hi_u32 s20, s13, 0xaaaaaaab
	s_lshr_b32 s42, s20, 1
	s_and_b64 s[6:7], s[18:19], s[6:7]
	s_add_i32 s20, s14, 0xffffffba
	s_cmpk_gt_i32 s20, 0x7e
	s_cselect_b64 s[34:35], -1, 0
	s_and_b64 s[6:7], s[34:35], s[6:7]
	s_cmpk_lt_i32 s14, 0x200
	s_cselect_b64 s[20:21], -1, 0
	s_mul_i32 s42, s42, 0x18000
	s_and_b64 s[38:39], s[6:7], s[20:21]
	v_cndmask_b32_e64 v5, 0, 1, s[18:19]
	v_subrev_u32_e32 v1, s42, v232
	v_subrev_u32_e32 v2, s42, v233
	v_subrev_u32_e32 v142, s42, v234
	v_subrev_u32_e32 v143, s42, v235
	s_mov_b64 s[6:7], -1
	s_andn2_b64 vcc, exec, s[38:39]
	v_cmp_ne_u32_e64 s[18:19], 1, v5
	s_cbranch_vccz .LBB0_1230
	s_and_b64 vcc, exec, s[18:19]
	v_mov_b64_e32 v[196:197], v[136:137]
	v_mov_b64_e32 v[198:199], v[134:135]
	s_cbranch_vccnz .LBB0_1217
	s_add_i32 s6, s15, s47
	v_add_u32_e32 v5, s6, v143
	v_add_u32_e32 v148, s6, v142
	v_add_u32_e32 v149, s6, v2
	v_add_u32_e32 v152, s6, v1
	ds_read_b128 v[38:41], v5
	ds_read_b128 v[42:45], v5 offset:4096
	ds_read_b128 v[118:121], v148
	ds_read_b128 v[122:125], v148 offset:4096
	ds_read_b128 v[126:129], v149
	ds_read_b128 v[138:141], v149 offset:4096
	ds_read_b128 v[130:133], v152
	ds_read_b128 v[144:147], v152 offset:4096
	s_setprio 1
	s_waitcnt lgkmcnt(7)
	v_mfma_f32_16x16x32_f16 v[38:41], v[38:41], v[6:9], 0
	s_waitcnt lgkmcnt(5)
	v_mfma_f32_16x16x32_f16 v[38:41], v[118:121], v[10:13], v[38:41]
	s_waitcnt lgkmcnt(3)
	v_mfma_f32_16x16x32_f16 v[38:41], v[126:129], v[14:17], v[38:41]
	s_waitcnt lgkmcnt(1)
	v_mfma_f32_16x16x32_f16 v[130:133], v[130:133], v[18:21], v[38:41]
	v_mfma_f32_16x16x32_f16 v[38:41], v[42:45], v[6:9], 0
	v_mfma_f32_16x16x32_f16 v[38:41], v[122:125], v[10:13], v[38:41]
	v_mfma_f32_16x16x32_f16 v[38:41], v[138:141], v[14:17], v[38:41]
	s_waitcnt lgkmcnt(0)
	v_mfma_f32_16x16x32_f16 v[126:129], v[144:147], v[18:21], v[38:41]
	s_setprio 0
	s_nop 5
	ds_read_b128 v[38:41], v5 offset:8192
	ds_read_b128 v[42:45], v5 offset:12288
	ds_read_b128 v[118:121], v148 offset:8192
	ds_read_b128 v[138:141], v148 offset:12288
	ds_read_b128 v[122:125], v149 offset:8192
	ds_read_b128 v[144:147], v149 offset:12288
	ds_read_b128 v[148:151], v152 offset:8192
	ds_read_b128 v[152:155], v152 offset:12288
	s_setprio 1
	s_waitcnt lgkmcnt(7)
	v_mfma_f32_16x16x32_f16 v[38:41], v[38:41], v[6:9], 0
	s_waitcnt lgkmcnt(5)
	v_mfma_f32_16x16x32_f16 v[38:41], v[118:121], v[10:13], v[38:41]
	s_waitcnt lgkmcnt(3)
	v_mfma_f32_16x16x32_f16 v[38:41], v[122:125], v[14:17], v[38:41]
	s_waitcnt lgkmcnt(1)
	v_mfma_f32_16x16x32_f16 v[122:125], v[148:151], v[18:21], v[38:41]
	v_mfma_f32_16x16x32_f16 v[38:41], v[42:45], v[6:9], 0
	v_mfma_f32_16x16x32_f16 v[38:41], v[138:141], v[10:13], v[38:41]
	v_mfma_f32_16x16x32_f16 v[38:41], v[144:147], v[14:17], v[38:41]
	s_waitcnt lgkmcnt(0)
	v_mfma_f32_16x16x32_f16 v[118:121], v[152:155], v[18:21], v[38:41]
	s_setprio 0
	s_add_i32 s6, s14, -4
	s_cmpk_lt_i32 s6, 0x200
	s_cselect_b64 s[6:7], -1, 0
	s_and_b64 s[6:7], s[34:35], s[6:7]
	s_andn2_b64 vcc, exec, s[6:7]
	s_mov_b64 s[6:7], -1
	s_cbranch_vccz .LBB0_1212
	v_add_u32_e32 v5, s14, v239
	v_add_u32_e32 v38, -7, v5
	v_add_u32_e32 v40, -8, v5
	v_add_u32_e32 v42, -9, v5
	v_add_u32_e32 v44, -10, v5
	v_add_u32_e32 v138, -11, v5
	v_add_u32_e32 v140, -12, v5
	v_add_u32_e32 v144, -13, v5
	v_med3_i32 v39, v38, 0, v243
	v_med3_i32 v41, v40, 0, v243
	v_med3_i32 v43, v42, 0, v243
	v_med3_i32 v45, v44, 0, v243
	v_med3_i32 v139, v138, 0, v243
	v_med3_i32 v141, v140, 0, v243
	v_med3_i32 v145, v144, 0, v243
	v_add_u32_e32 v148, -14, v5
	v_lshl_add_u32 v39, v39, 2, v244
	v_lshl_add_u32 v41, v41, 2, v244
	v_lshl_add_u32 v43, v43, 2, v244
	v_lshl_add_u32 v45, v45, 2, v244
	v_lshl_add_u32 v139, v139, 2, v244
	v_lshl_add_u32 v141, v141, 2, v244
	v_lshl_add_u32 v145, v145, 2, v244
	v_med3_i32 v146, v148, 0, v243
	v_subrev_u32_e32 v150, 39, v5
	v_subrev_u32_e32 v152, 41, v5
	v_subrev_u32_e32 v154, 42, v5
	v_subrev_u32_e32 v156, 43, v5
	v_subrev_u32_e32 v158, 44, v5
	v_subrev_u32_e32 v160, 45, v5
	v_lshl_add_u32 v146, v146, 2, v244
	ds_read_b32 v39, v39
	ds_read_b32 v41, v41
	ds_read_b32 v43, v43
	ds_read_b32 v45, v45
	ds_read_b32 v139, v139
	ds_read_b32 v141, v141
	ds_read_b32 v147, v145
	ds_read_b32 v149, v146
	v_med3_i32 v145, v150, 0, v243
	v_subrev_u32_e32 v151, 40, v5
	v_med3_i32 v153, v152, 0, v243
	v_med3_i32 v155, v154, 0, v243
	v_med3_i32 v157, v156, 0, v243
	v_med3_i32 v159, v158, 0, v243
	v_med3_i32 v161, v160, 0, v243
	v_subrev_u32_e32 v162, 46, v5
	v_lshl_add_u32 v145, v145, 2, v244
	v_med3_i32 v146, v151, 0, v243
	v_lshl_add_u32 v153, v153, 2, v244
	v_lshl_add_u32 v155, v155, 2, v244
	v_lshl_add_u32 v157, v157, 2, v244
	v_lshl_add_u32 v159, v159, 2, v244
	v_lshl_add_u32 v161, v161, 2, v244
	v_med3_i32 v5, v162, 0, v243
	v_lshl_add_u32 v146, v146, 2, v244
	v_lshl_add_u32 v5, v5, 2, v244
	ds_read_b32 v163, v145
	ds_read_b32 v164, v146
	ds_read_b32 v153, v153
	ds_read_b32 v155, v155
	ds_read_b32 v157, v157
	ds_read_b32 v159, v159
	ds_read_b32 v161, v161
	ds_read_b32 v165, v5
	s_waitcnt lgkmcnt(0)
	v_fmac_f32_e32 v39, 0x3e0293ee, v130
	v_cmp_gt_u32_e32 vcc, s62, v38
	v_fmac_f32_e32 v41, 0x3e0293ee, v131
	v_fmac_f32_e32 v43, 0x3e0293ee, v132
	v_cndmask_b32_e32 v38, v241, v39, vcc
	v_cmp_gt_u32_e32 vcc, s62, v40
	v_fmac_f32_e32 v45, 0x3e0293ee, v133
	v_fmac_f32_e32 v139, 0x3e0293ee, v126
	v_cndmask_b32_e32 v39, v241, v41, vcc
	v_cmp_gt_u32_e32 vcc, s62, v42
	v_fmac_f32_e32 v141, 0x3e0293ee, v127
	v_fmac_f32_e32 v147, 0x3e0293ee, v128
	v_cndmask_b32_e32 v41, v241, v43, vcc
	v_cmp_gt_u32_e32 vcc, s62, v44
	v_fmac_f32_e32 v149, 0x3e0293ee, v129
	v_fmac_f32_e32 v163, 0x3e0293ee, v122
	v_cndmask_b32_e32 v146, v241, v45, vcc
	v_cmp_gt_u32_e32 vcc, s62, v138
	v_fmac_f32_e32 v164, 0x3e0293ee, v123
	v_fmac_f32_e32 v153, 0x3e0293ee, v124
	v_cndmask_b32_e32 v40, v241, v139, vcc
	v_cmp_gt_u32_e32 vcc, s62, v140
	v_max_f32_e32 v42, v38, v39
	v_fmac_f32_e32 v155, 0x3e0293ee, v125
	v_cndmask_b32_e32 v145, v241, v141, vcc
	v_cmp_gt_u32_e32 vcc, s62, v144
	v_max3_f32 v42, v42, v41, v146
	v_fmac_f32_e32 v157, 0x3e0293ee, v118
	v_cndmask_b32_e32 v147, v241, v147, vcc
	v_cmp_gt_u32_e32 vcc, s62, v148
	v_max3_f32 v42, v42, v40, v145
	v_fmac_f32_e32 v159, 0x3e0293ee, v119
	v_cndmask_b32_e32 v148, v241, v149, vcc
	v_cmp_gt_u32_e32 vcc, s62, v150
	v_max3_f32 v42, v42, v147, v148
	v_fmac_f32_e32 v161, 0x3e0293ee, v120
	v_cndmask_b32_e32 v5, v241, v163, vcc
	v_cmp_gt_u32_e32 vcc, s62, v151
	v_fmac_f32_e32 v165, 0x3e0293ee, v121
	v_add_f32_e32 v43, 0x41000000, v136
	v_cndmask_b32_e32 v44, v241, v164, vcc
	v_cmp_gt_u32_e32 vcc, s62, v152
	v_max3_f32 v42, v42, v5, v44
	s_nop 0
	v_cndmask_b32_e32 v138, v241, v153, vcc
	v_cmp_gt_u32_e32 vcc, s62, v154
	s_nop 1
	v_cndmask_b32_e32 v140, v241, v155, vcc
	v_cmp_gt_u32_e32 vcc, s62, v156
	v_max3_f32 v42, v42, v138, v140
	s_nop 0
	v_cndmask_b32_e32 v45, v241, v157, vcc
	v_cmp_gt_u32_e32 vcc, s62, v158
	s_nop 1
	v_cndmask_b32_e32 v139, v241, v159, vcc
	v_cmp_gt_u32_e32 vcc, s62, v160
	v_max3_f32 v42, v42, v45, v139
	s_nop 0
	v_cndmask_b32_e32 v141, v241, v161, vcc
	v_cmp_gt_u32_e32 vcc, s62, v162
	s_nop 1
	v_cndmask_b32_e32 v144, v241, v165, vcc
	v_max3_f32 v42, v42, v141, v144
	v_cmp_gt_f32_e32 vcc, v42, v43
	s_cbranch_vccz .LBB0_1210
	ds_bpermute_b32 v43, v245, v42
	v_max_f32_e32 v42, v42, v42
	s_waitcnt lgkmcnt(0)
	v_max_f32_e32 v43, v43, v43
	v_max_f32_e32 v42, v42, v43
	ds_bpermute_b32 v43, v246, v42
	s_waitcnt lgkmcnt(0)
	v_max3_f32 v42, v136, v42, v43
	v_sub_f32_e32 v43, v136, v42
	v_exp_f32_e32 v194, v43
	v_mov_b32_e32 v43, v137
	v_mov_b64_e32 v[196:197], v[42:43]
	s_branch .LBB0_1211

.LBB0_1217:
	s_andn2_b64 vcc, exec, s[36:37]
	s_cbranch_vccnz .LBB0_1229
	s_add_i32 s6, s15, s47
	v_add_u32_e32 v4, s6, v143
	v_add_u32_e32 v5, s6, v142
	v_add_u32_e32 v148, s6, v2
	v_add_u32_e32 v152, s6, v1
	ds_read_b128 v[46:49], v4
	ds_read_b128 v[50:53], v4 offset:4096
	ds_read_b128 v[118:121], v5
	ds_read_b128 v[122:125], v5 offset:4096
	ds_read_b128 v[126:129], v148
	ds_read_b128 v[138:141], v148 offset:4096
	ds_read_b128 v[130:133], v152
	ds_read_b128 v[144:147], v152 offset:4096
	s_setprio 1
	s_waitcnt lgkmcnt(7)
	v_mfma_f32_16x16x32_f16 v[46:49], v[46:49], v[22:25], 0
	s_waitcnt lgkmcnt(5)
	v_mfma_f32_16x16x32_f16 v[46:49], v[118:121], v[26:29], v[46:49]
	s_waitcnt lgkmcnt(3)
	v_mfma_f32_16x16x32_f16 v[46:49], v[126:129], v[30:33], v[46:49]
	s_waitcnt lgkmcnt(1)
	v_mfma_f32_16x16x32_f16 v[130:133], v[130:133], v[34:37], v[46:49]
	v_mfma_f32_16x16x32_f16 v[46:49], v[50:53], v[22:25], 0
	v_mfma_f32_16x16x32_f16 v[46:49], v[122:125], v[26:29], v[46:49]
	v_mfma_f32_16x16x32_f16 v[46:49], v[138:141], v[30:33], v[46:49]
	s_waitcnt lgkmcnt(0)
	v_mfma_f32_16x16x32_f16 v[126:129], v[144:147], v[34:37], v[46:49]
	s_setprio 0
	s_nop 5
	ds_read_b128 v[46:49], v4 offset:8192
	ds_read_b128 v[50:53], v4 offset:12288
	ds_read_b128 v[118:121], v5 offset:8192
	ds_read_b128 v[138:141], v5 offset:12288
	ds_read_b128 v[122:125], v148 offset:8192
	ds_read_b128 v[144:147], v148 offset:12288
	ds_read_b128 v[148:151], v152 offset:8192
	ds_read_b128 v[152:155], v152 offset:12288
	s_setprio 1
	s_waitcnt lgkmcnt(7)
	v_mfma_f32_16x16x32_f16 v[46:49], v[46:49], v[22:25], 0
	s_waitcnt lgkmcnt(5)
	v_mfma_f32_16x16x32_f16 v[46:49], v[118:121], v[26:29], v[46:49]
	s_waitcnt lgkmcnt(3)
	v_mfma_f32_16x16x32_f16 v[46:49], v[122:125], v[30:33], v[46:49]
	s_waitcnt lgkmcnt(1)
	v_mfma_f32_16x16x32_f16 v[122:125], v[148:151], v[34:37], v[46:49]
	v_mfma_f32_16x16x32_f16 v[46:49], v[50:53], v[22:25], 0
	v_mfma_f32_16x16x32_f16 v[46:49], v[138:141], v[26:29], v[46:49]
	v_mfma_f32_16x16x32_f16 v[46:49], v[144:147], v[30:33], v[46:49]
	s_waitcnt lgkmcnt(0)
	v_mfma_f32_16x16x32_f16 v[118:121], v[152:155], v[34:37], v[46:49]
	s_setprio 0
	s_add_i32 s6, s14, 0xffffffbe
	s_cmpk_gt_i32 s6, 0x7e
	s_cselect_b64 s[6:7], -1, 0
	s_and_b64 s[20:21], s[6:7], s[20:21]
	s_mov_b64 s[6:7], -1
	s_and_b64 vcc, exec, s[20:21]
	s_cbranch_vccnz .LBB0_1223
	v_add_u32_e32 v4, s14, v239
	v_add_u32_e32 v5, -3, v4
	v_max_i32_e32 v47, 1, v5
	v_add_u32_e32 v47, -1, v47
	v_add_u32_e32 v48, -5, v4
	v_add_u32_e32 v50, -6, v4
	v_add_u32_e32 v52, -7, v4
	v_add_u32_e32 v138, -8, v4
	v_add_u32_e32 v140, -9, v4
	v_add_u32_e32 v144, -10, v4
	v_subrev_u32_e32 v146, 35, v4
	v_subrev_u32_e32 v151, 36, v4
	v_subrev_u32_e32 v152, 37, v4
	v_subrev_u32_e32 v153, 38, v4
	v_subrev_u32_e32 v154, 39, v4
	v_subrev_u32_e32 v156, 40, v4
	v_subrev_u32_e32 v158, 41, v4
	v_subrev_u32_e32 v4, 42, v4
	v_med3_i32 v46, v5, 0, v243
	v_min_u32_e32 v47, 0x7f, v47
	v_med3_i32 v49, v48, 0, v243
	v_med3_i32 v51, v50, 0, v243
	v_med3_i32 v53, v52, 0, v243
	v_med3_i32 v139, v138, 0, v243
	v_med3_i32 v141, v140, 0, v243
	v_med3_i32 v145, v144, 0, v243
	v_med3_i32 v147, v146, 0, v243
	v_med3_i32 v155, v154, 0, v243
	v_med3_i32 v157, v156, 0, v243
	v_med3_i32 v159, v158, 0, v243
	v_med3_i32 v160, v4, 0, v243
	v_lshl_add_u32 v46, v46, 2, v244
	v_lshl_add_u32 v47, v47, 2, v244
	v_lshl_add_u32 v49, v49, 2, v244
	v_lshl_add_u32 v51, v51, 2, v244
	v_lshl_add_u32 v53, v53, 2, v244
	v_lshl_add_u32 v139, v139, 2, v244
	v_lshl_add_u32 v141, v141, 2, v244
	v_lshl_add_u32 v145, v145, 2, v244
	v_lshl_add_u32 v147, v147, 2, v244
	v_med3_i32 v148, v151, 0, v243
	v_med3_i32 v149, v152, 0, v243
	v_med3_i32 v150, v153, 0, v243
	v_lshl_add_u32 v155, v155, 2, v244
	v_lshl_add_u32 v157, v157, 2, v244
	v_lshl_add_u32 v159, v159, 2, v244
	v_lshl_add_u32 v160, v160, 2, v244
	ds_read_b32 v46, v46
	ds_read_b32 v47, v47
	ds_read_b32 v49, v49
	ds_read_b32 v51, v51
	ds_read_b32 v53, v53
	ds_read_b32 v139, v139
	ds_read_b32 v141, v141
	ds_read_b32 v145, v145
	v_lshl_add_u32 v148, v148, 2, v244
	v_lshl_add_u32 v149, v149, 2, v244
	v_lshl_add_u32 v150, v150, 2, v244
	ds_read_b32 v161, v147
	ds_read_b32 v162, v148
	ds_read_b32 v163, v149
	ds_read_b32 v164, v150
	ds_read_b32 v155, v155
	ds_read_b32 v157, v157
	ds_read_b32 v159, v159
	ds_read_b32 v160, v160
	s_waitcnt lgkmcnt(0)
	v_fmac_f32_e32 v46, 0x3e0293ee, v130
	v_cmp_gt_u32_e32 vcc, s62, v5
	s_movk_i32 s6, 0x201
	v_fmac_f32_e32 v47, 0x3e0293ee, v131
	v_cndmask_b32_e32 v46, v241, v46, vcc
	v_cmp_gt_u32_e32 vcc, s6, v5
	v_fmac_f32_e32 v49, 0x3e0293ee, v132
	v_fmac_f32_e32 v51, 0x3e0293ee, v133
	v_cndmask_b32_e32 v47, v241, v47, vcc
	v_cmp_gt_u32_e32 vcc, s62, v48
	v_fmac_f32_e32 v53, 0x3e0293ee, v126
	v_fmac_f32_e32 v139, 0x3e0293ee, v127
	v_cndmask_b32_e32 v49, v241, v49, vcc
	v_cmp_gt_u32_e32 vcc, s62, v50
	v_fmac_f32_e32 v141, 0x3e0293ee, v128
	v_fmac_f32_e32 v145, 0x3e0293ee, v129
	v_cndmask_b32_e32 v148, v241, v51, vcc
	v_cmp_gt_u32_e32 vcc, s62, v52
	v_fmac_f32_e32 v161, 0x3e0293ee, v122
	v_fmac_f32_e32 v162, 0x3e0293ee, v123
	v_cndmask_b32_e32 v48, v241, v53, vcc
	v_cmp_gt_u32_e32 vcc, s62, v138
	v_fmac_f32_e32 v163, 0x3e0293ee, v124
	v_fmac_f32_e32 v164, 0x3e0293ee, v125
	v_cndmask_b32_e32 v147, v241, v139, vcc
	v_cmp_gt_u32_e32 vcc, s62, v140
	v_fmac_f32_e32 v155, 0x3e0293ee, v118
	v_fmac_f32_e32 v157, 0x3e0293ee, v119
	v_cndmask_b32_e32 v149, v241, v141, vcc
	v_cmp_gt_u32_e32 vcc, s62, v144
	v_fmac_f32_e32 v159, 0x3e0293ee, v120
	v_fmac_f32_e32 v160, 0x3e0293ee, v121
	v_cndmask_b32_e32 v150, v241, v145, vcc
	v_cmp_gt_u32_e32 vcc, s62, v146
	v_add_f32_e32 v50, 0x41000000, v197
	s_nop 0
	v_cndmask_b32_e32 v5, v241, v161, vcc
	v_cmp_gt_u32_e32 vcc, s62, v151
	s_nop 1
	v_cndmask_b32_e32 v52, v241, v162, vcc
	v_cmp_gt_u32_e32 vcc, s62, v152
	s_nop 1
	v_cndmask_b32_e32 v140, v241, v163, vcc
	v_cmp_gt_u32_e32 vcc, s62, v153
	s_nop 1
	v_cndmask_b32_e32 v144, v241, v164, vcc
	v_cmp_gt_u32_e32 vcc, s62, v154
	s_nop 1
	v_cndmask_b32_e32 v53, v241, v155, vcc
	v_cmp_gt_u32_e32 vcc, s62, v156
	s_nop 1
	v_cndmask_b32_e32 v141, v241, v157, vcc
	v_cmp_gt_u32_e32 vcc, s62, v158
	s_nop 1
	v_cndmask_b32_e32 v145, v241, v159, vcc
	v_cmp_gt_u32_e32 vcc, s62, v4
	v_max_f32_e32 v4, v46, v47
	v_max3_f32 v4, v4, v49, v148
	v_max3_f32 v4, v4, v48, v147
	v_max3_f32 v4, v4, v149, v150
	v_max3_f32 v4, v4, v5, v52
	v_max3_f32 v4, v4, v140, v144
	v_cndmask_b32_e32 v146, v241, v160, vcc
	v_max3_f32 v4, v4, v53, v141
	v_max3_f32 v4, v4, v145, v146
	v_cmp_gt_f32_e32 vcc, v4, v50
	s_cbranch_vccz .LBB0_1221
	ds_bpermute_b32 v50, v245, v4
	v_max_f32_e32 v4, v4, v4
	s_waitcnt lgkmcnt(0)
	v_max_f32_e32 v50, v50, v50
	v_max_f32_e32 v4, v4, v50
	ds_bpermute_b32 v50, v246, v4
	s_waitcnt lgkmcnt(0)
	v_max3_f32 v51, v197, v4, v50
	v_sub_f32_e32 v4, v197, v51
	v_exp_f32_e32 v4, v4
	v_mov_b32_e32 v50, v196
	v_mov_b64_e32 v[138:139], v[50:51]
	s_branch .LBB0_1222
